# strategy 7 (instruction selection): 50 intra-wave reduction steps moved from ds_swizzle round trips to DPP (quad_perm / row_half_mirror / row_mirror) in LN1, router top-k, combine and the attention la
# speedup vs baseline: 1.0107x; 1.0063x over previous
.Lattn_prio_done:
	v_readlane_b32 s20, v254, 55
	v_readlane_b32 s21, v254, 56
	s_add_u32 s8, s20, 0x2a200000
	s_addc_u32 s9, s21, 0
	s_add_u32 s4, s20, 0x48200000
	s_addc_u32 s5, s21, 0
	s_lshl_b64 s[6:7], s[74:75], 11
	v_readlane_b32 s40, v254, 57
	v_readlane_b32 s41, v254, 58
	s_add_u32 s10, s40, s6
	s_addc_u32 s11, s41, s7
	v_ashrrev_i32_e32 v143, 31, v142
	v_lshl_add_u64 v[2:3], v[142:143], 2, s[10:11]
	global_load_dword v0, v[2:3], off
	global_load_dword v4, v[2:3], off offset:512
	global_load_dword v5, v[2:3], off offset:256
	global_load_dword v6, v[2:3], off offset:768
	v_writelane_b32 v255, s4, 10
	v_readlane_b32 s42, v254, 59
	s_lshl_b64 s[6:7], s[74:75], 10
	v_writelane_b32 v255, s5, 11
	v_readlane_b32 s43, v254, 60
	s_add_u32 s4, s42, s6
	s_addc_u32 s5, s43, s7
	v_readlane_b32 s47, v255, 0
	v_writelane_b32 v255, s4, 12
	s_mov_b32 s6, 0x42b17218
	s_lshl_b32 s30, s74, 6
	v_writelane_b32 v255, s5, 13
	s_mov_b32 s4, 0x3fb8aa3b
	s_mov_b32 s5, 0xc2ce8ed0
	s_lshl_b64 s[10:11], s[30:31], 2
	s_add_u32 s10, s20, s10
	s_addc_u32 s11, s21, s11
	v_cmp_eq_u32_e64 s[38:39], 0, v178
	v_readlane_b32 s44, v254, 61
	v_readlane_b32 s45, v254, 62
	v_readlane_b32 s46, v254, 63
	s_waitcnt vmcnt(0)
	v_mul_f32_e32 v5, v5, v6
	v_fmac_f32_e32 v5, v0, v4
	s_nop 1
	s_waitcnt lgkmcnt(0)
	v_add_f32_dpp v0, v5, v5 quad_perm:[1,0,3,2] row_mask:0xf bank_mask:0xf
	s_nop 1
	s_waitcnt lgkmcnt(0)
	v_add_f32_dpp v0, v0, v0 quad_perm:[2,3,0,1] row_mask:0xf bank_mask:0xf
	s_nop 1
	s_waitcnt lgkmcnt(0)
	v_add_f32_dpp v0, v0, v0 row_half_mirror row_mask:0xf bank_mask:0xf
	s_nop 1
	s_waitcnt lgkmcnt(0)
	v_add_f32_dpp v0, v0, v0 row_mirror row_mask:0xf bank_mask:0xf
	ds_swizzle_b32 v4, v0 offset:swizzle(SWAP,16)
	s_waitcnt lgkmcnt(0)
	v_add_f32_e32 v0, v0, v4
	v_mov_b32_e32 v4, v0
	s_nop 1
	v_permlane32_swap_b32_e32 v0, v4
	v_add_f32_e32 v0, v0, v4
	global_load_dword v4, v[2:3], off offset:1024
	global_load_dword v5, v[2:3], off offset:1536
	global_load_dword v6, v[2:3], off offset:1280
	s_nop 0
	global_load_dword v2, v[2:3], off offset:1792
	s_waitcnt vmcnt(0)
	v_mul_f32_e32 v2, v6, v2
	v_fmac_f32_e32 v2, v4, v5
	s_nop 1
	s_waitcnt lgkmcnt(0)
	v_add_f32_dpp v2, v2, v2 quad_perm:[1,0,3,2] row_mask:0xf bank_mask:0xf
	s_nop 1
	s_waitcnt lgkmcnt(0)
	v_add_f32_dpp v2, v2, v2 quad_perm:[2,3,0,1] row_mask:0xf bank_mask:0xf
	s_nop 1
	s_waitcnt lgkmcnt(0)
	v_add_f32_dpp v2, v2, v2 row_half_mirror row_mask:0xf bank_mask:0xf
	s_nop 1
	s_waitcnt lgkmcnt(0)
	v_add_f32_dpp v2, v2, v2 row_mirror row_mask:0xf bank_mask:0xf
	ds_swizzle_b32 v3, v2 offset:swizzle(SWAP,16)
	s_waitcnt lgkmcnt(0)
	v_add_f32_e32 v2, v2, v3
	v_mov_b32_e32 v3, v2
	s_nop 1
	v_permlane32_swap_b32_e32 v2, v3
	v_add_f32_e32 v2, v2, v3
	v_cvt_f32_u32_e32 v3, s74
	v_mul_f32_e32 v3, 0xbe99999a, v3
	v_mul_f32_e32 v4, 0x3fb8aa3b, v3
	v_fma_f32 v5, v3, s4, -v4
	v_rndne_f32_e32 v6, v4
	v_fmac_f32_e32 v5, 0x32a5705f, v3
	v_sub_f32_e32 v4, v4, v6
	v_add_f32_e32 v4, v4, v5
	v_exp_f32_e32 v4, v4
	v_cvt_i32_f32_e32 v5, v6
	v_cmp_ngt_f32_e32 vcc, s5, v3
	v_ldexp_f32 v4, v4, v5
	s_nop 0
	v_cndmask_b32_e32 v4, 0, v4, vcc
	v_cmp_nlt_f32_e32 vcc, s6, v3
	s_nop 1
	v_cndmask_b32_e32 v3, v231, v4, vcc
	v_mov_b32_e32 v4, 0x3f4ccccd
	v_fmamk_f32 v3, v3, 0xbf19999a, v4
	v_mul_f32_e32 v4, 0x3fb8aa3b, v0
	v_fma_f32 v5, v0, s4, -v4
	v_rndne_f32_e32 v6, v4
	v_fmac_f32_e32 v5, 0x32a5705f, v0
	v_sub_f32_e32 v4, v4, v6
	v_add_f32_e32 v4, v4, v5
	v_exp_f32_e32 v4, v4
	v_cvt_i32_f32_e32 v5, v6
	v_cmp_ngt_f32_e32 vcc, s5, v0
	v_sub_f32_e32 v227, 1.0, v3
	v_ldexp_f32 v4, v4, v5
	v_cndmask_b32_e32 v4, 0, v4, vcc
	v_cmp_nlt_f32_e32 vcc, s6, v0
	s_nop 1
	v_cndmask_b32_e32 v0, v231, v4, vcc
	v_mul_f32_e32 v4, 0x3fb8aa3b, v2
	v_fma_f32 v5, v2, s4, -v4
	v_rndne_f32_e32 v6, v4
	v_fmac_f32_e32 v5, 0x32a5705f, v2
	v_sub_f32_e32 v4, v4, v6
	v_add_f32_e32 v4, v4, v5
	v_exp_f32_e32 v4, v4
	v_cvt_i32_f32_e32 v5, v6
	v_cmp_ngt_f32_e32 vcc, s5, v2
	v_ldexp_f32 v4, v4, v5
	s_nop 0
	v_cndmask_b32_e32 v4, 0, v4, vcc
	v_cmp_nlt_f32_e32 vcc, s6, v2
	s_nop 1
	v_cndmask_b32_e32 v2, v231, v4, vcc
	v_sub_f32_e32 v0, v0, v2
	v_add_f32_e32 v0, v3, v0
	s_nop 0
	v_readfirstlane_b32 s4, v0
	s_nop 1
	v_writelane_b32 v255, s4, 14
	s_add_u32 s4, s10, 0x10000
	s_addc_u32 s5, s11, 0
	v_writelane_b32 v255, s4, 15
	s_nop 1
	v_writelane_b32 v255, s5, 16
	s_branch .LBB0_262

.LBB0_881:
	s_or_b32 s64, s6, s72
	s_ashr_i32 s65, s64, 31
	s_lshl_b64 s[6:7], s[64:65], 12
	v_lshl_add_u64 v[56:57], v[84:85], 0, s[6:7]
	global_load_dwordx4 v[58:61], v[56:57], off
	global_load_dwordx4 v[62:65], v[56:57], off offset:1024
	global_load_dwordx4 v[166:169], v[56:57], off offset:2048
	global_load_dwordx4 v[170:173], v[56:57], off offset:3072
	s_or_b32 s62, s64, 1
	s_ashr_i32 s63, s62, 31
	s_or_b32 s60, s64, 2
	s_lshl_b64 s[6:7], s[62:63], 12
	s_ashr_i32 s61, s60, 31
	v_lshl_add_u64 v[54:55], v[84:85], 0, s[6:7]
	s_lshl_b64 s[6:7], s[60:61], 12
	v_lshl_add_u64 v[52:53], v[84:85], 0, s[6:7]
	s_or_b32 s6, s64, 3
	s_ashr_i32 s7, s6, 31
	s_lshl_b64 s[20:21], s[6:7], 12
	v_lshl_add_u64 v[50:51], v[84:85], 0, s[20:21]
	global_load_dwordx4 v[46:49], v[54:55], off
	global_load_dwordx4 v[42:45], v[54:55], off offset:1024
	global_load_dwordx4 v[38:41], v[54:55], off offset:2048
	global_load_dwordx4 v[34:37], v[54:55], off offset:3072
	global_load_dwordx4 v[30:33], v[52:53], off
	global_load_dwordx4 v[26:29], v[52:53], off offset:1024
	global_load_dwordx4 v[22:25], v[52:53], off offset:2048
	global_load_dwordx4 v[18:21], v[52:53], off offset:3072
	global_load_dwordx4 v[14:17], v[50:51], off
	global_load_dwordx4 v[10:13], v[50:51], off offset:1024
	global_load_dwordx4 v[6:9], v[50:51], off offset:2048
	global_load_dwordx4 v[2:5], v[50:51], off offset:3072
	s_lshl_b64 s[6:7], s[6:7], 11
	s_waitcnt vmcnt(15)
	v_lshlrev_b32_e32 v164, 16, v58
	v_and_b32_e32 v163, 0xffff0000, v58
	v_lshlrev_b32_e32 v162, 16, v59
	v_and_b32_e32 v161, 0xffff0000, v59
	v_lshlrev_b32_e32 v160, 16, v60
	v_and_b32_e32 v159, 0xffff0000, v60
	v_lshlrev_b32_e32 v111, 16, v61
	v_and_b32_e32 v110, 0xffff0000, v61
	v_add_f32_e32 v0, v164, v163
	v_add_f32_e32 v58, v162, v161
	v_add_f32_e32 v0, v0, v58
	v_add_f32_e32 v58, v160, v159
	v_add_f32_e32 v59, v111, v110
	v_add_f32_e32 v58, v58, v59
	s_waitcnt vmcnt(14)
	v_lshlrev_b32_e32 v109, 16, v62
	v_and_b32_e32 v108, 0xffff0000, v62
	v_lshlrev_b32_e32 v107, 16, v63
	v_and_b32_e32 v106, 0xffff0000, v63
	v_add_f32_e32 v0, v0, v58
	v_lshlrev_b32_e32 v105, 16, v64
	v_and_b32_e32 v104, 0xffff0000, v64
	v_lshlrev_b32_e32 v103, 16, v65
	v_and_b32_e32 v102, 0xffff0000, v65
	v_add_f32_e32 v58, v109, v108
	v_add_f32_e32 v59, v107, v106
	v_add_f32_e32 v58, v58, v59
	v_add_f32_e32 v59, v105, v104
	v_add_f32_e32 v60, v103, v102
	v_add_f32_e32 v59, v59, v60
	v_add_f32_e32 v0, 0, v0
	v_add_f32_e32 v58, v58, v59
	s_waitcnt vmcnt(13)
	v_lshlrev_b32_e32 v101, 16, v166
	v_and_b32_e32 v100, 0xffff0000, v166
	v_lshlrev_b32_e32 v99, 16, v167
	v_and_b32_e32 v98, 0xffff0000, v167
	v_add_f32_e32 v0, v0, v58
	v_lshlrev_b32_e32 v97, 16, v168
	v_and_b32_e32 v96, 0xffff0000, v168
	v_lshlrev_b32_e32 v95, 16, v169
	v_and_b32_e32 v94, 0xffff0000, v169
	v_add_f32_e32 v58, v101, v100
	v_add_f32_e32 v59, v99, v98
	v_add_f32_e32 v58, v58, v59
	v_add_f32_e32 v59, v97, v96
	v_add_f32_e32 v60, v95, v94
	v_add_f32_e32 v59, v59, v60
	v_add_f32_e32 v58, v58, v59
	s_waitcnt vmcnt(12)
	v_lshlrev_b32_e32 v67, 16, v170
	v_and_b32_e32 v65, 0xffff0000, v170
	v_lshlrev_b32_e32 v64, 16, v171
	v_and_b32_e32 v63, 0xffff0000, v171
	v_add_f32_e32 v58, v0, v58
	v_lshlrev_b32_e32 v62, 16, v172
	v_and_b32_e32 v61, 0xffff0000, v172
	v_lshlrev_b32_e32 v60, 16, v173
	v_and_b32_e32 v0, 0xffff0000, v173
	v_add_f32_e32 v59, v67, v65
	v_add_f32_e32 v91, v64, v63
	v_add_f32_e32 v59, v59, v91
	v_add_f32_e32 v91, v62, v61
	v_add_f32_e32 v165, v60, v0
	v_add_f32_e32 v91, v91, v165
	v_add_f32_e32 v59, v59, v91
	v_add_f32_e32 v58, v58, v59
	s_nop 1
	s_waitcnt lgkmcnt(0)
	v_add_f32_dpp v58, v58, v58 quad_perm:[1,0,3,2] row_mask:0xf bank_mask:0xf
	s_nop 1
	s_waitcnt lgkmcnt(0)
	v_add_f32_dpp v58, v58, v58 quad_perm:[2,3,0,1] row_mask:0xf bank_mask:0xf
	s_nop 1
	s_waitcnt lgkmcnt(0)
	v_add_f32_dpp v58, v58, v58 row_half_mirror row_mask:0xf bank_mask:0xf
	s_nop 1
	s_waitcnt lgkmcnt(0)
	v_add_f32_dpp v58, v58, v58 row_mirror row_mask:0xf bank_mask:0xf
	ds_swizzle_b32 v59, v58 offset:swizzle(SWAP,16)
	s_waitcnt lgkmcnt(0)
	v_add_f32_e32 v58, v58, v59
	v_mov_b32_e32 v59, v58
	s_nop 1
	v_permlane32_swap_b32_e32 v58, v59
	v_add_f32_e32 v58, v58, v59
	v_fmac_f32_e32 v163, 0xba000000, v58
	v_fmac_f32_e32 v164, 0xba000000, v58
	v_mul_f32_e32 v59, v163, v163
	v_fmac_f32_e32 v59, v164, v164
	v_fmac_f32_e32 v162, 0xba000000, v58
	v_fmac_f32_e32 v59, v162, v162
	v_fmac_f32_e32 v161, 0xba000000, v58
	v_fmac_f32_e32 v59, v161, v161
	v_fmac_f32_e32 v160, 0xba000000, v58
	v_fmac_f32_e32 v59, v160, v160
	v_fmac_f32_e32 v159, 0xba000000, v58
	v_fmac_f32_e32 v59, v159, v159
	v_fmac_f32_e32 v111, 0xba000000, v58
	v_fmac_f32_e32 v59, v111, v111
	v_fmac_f32_e32 v110, 0xba000000, v58
	v_fmac_f32_e32 v59, v110, v110
	v_fmac_f32_e32 v109, 0xba000000, v58
	v_fmac_f32_e32 v59, v109, v109
	v_fmac_f32_e32 v108, 0xba000000, v58
	v_fmac_f32_e32 v59, v108, v108
	v_fmac_f32_e32 v107, 0xba000000, v58
	v_fmac_f32_e32 v59, v107, v107
	v_fmac_f32_e32 v106, 0xba000000, v58
	v_fmac_f32_e32 v59, v106, v106
	v_fmac_f32_e32 v105, 0xba000000, v58
	v_fmac_f32_e32 v59, v105, v105
	v_fmac_f32_e32 v104, 0xba000000, v58
	v_fmac_f32_e32 v59, v104, v104
	v_fmac_f32_e32 v103, 0xba000000, v58
	v_fmac_f32_e32 v59, v103, v103
	v_fmac_f32_e32 v102, 0xba000000, v58
	v_fmac_f32_e32 v59, v102, v102
	v_fmac_f32_e32 v101, 0xba000000, v58
	v_fmac_f32_e32 v59, v101, v101
	v_fmac_f32_e32 v100, 0xba000000, v58
	v_fmac_f32_e32 v59, v100, v100
	v_fmac_f32_e32 v99, 0xba000000, v58
	v_fmac_f32_e32 v59, v99, v99
	v_fmac_f32_e32 v98, 0xba000000, v58
	v_fmac_f32_e32 v59, v98, v98
	v_fmac_f32_e32 v97, 0xba000000, v58
	v_fmac_f32_e32 v59, v97, v97
	v_fmac_f32_e32 v96, 0xba000000, v58
	v_fmac_f32_e32 v59, v96, v96
	v_fmac_f32_e32 v95, 0xba000000, v58
	v_fmac_f32_e32 v59, v95, v95
	v_fmac_f32_e32 v94, 0xba000000, v58
	v_fmac_f32_e32 v59, v94, v94
	v_fmac_f32_e32 v67, 0xba000000, v58
	v_fmac_f32_e32 v59, v67, v67
	v_fmac_f32_e32 v65, 0xba000000, v58
	v_fmac_f32_e32 v59, v65, v65
	v_fmac_f32_e32 v64, 0xba000000, v58
	v_fmac_f32_e32 v59, v64, v64
	v_fmac_f32_e32 v63, 0xba000000, v58
	v_fmac_f32_e32 v59, v63, v63
	v_fmac_f32_e32 v62, 0xba000000, v58
	v_fmac_f32_e32 v59, v62, v62
	v_fmac_f32_e32 v61, 0xba000000, v58
	v_fmac_f32_e32 v59, v61, v61
	v_fmac_f32_e32 v60, 0xba000000, v58
	v_fmac_f32_e32 v59, v60, v60
	v_fmac_f32_e32 v0, 0xba000000, v58
	v_fmac_f32_e32 v59, v0, v0
	s_nop 1
	s_waitcnt lgkmcnt(0)
	v_add_f32_dpp v58, v59, v59 quad_perm:[1,0,3,2] row_mask:0xf bank_mask:0xf
	s_nop 1
	s_waitcnt lgkmcnt(0)
	v_add_f32_dpp v58, v58, v58 quad_perm:[2,3,0,1] row_mask:0xf bank_mask:0xf
	s_nop 1
	s_waitcnt lgkmcnt(0)
	v_add_f32_dpp v58, v58, v58 row_half_mirror row_mask:0xf bank_mask:0xf
	s_nop 1
	s_waitcnt lgkmcnt(0)
	v_add_f32_dpp v58, v58, v58 row_mirror row_mask:0xf bank_mask:0xf
	ds_swizzle_b32 v59, v58 offset:swizzle(SWAP,16)
	s_waitcnt lgkmcnt(0)
	v_add_f32_e32 v58, v58, v59
	v_mov_b32_e32 v59, v58
	s_nop 1
	v_permlane32_swap_b32_e32 v58, v59
	v_add_f32_e32 v58, v58, v59
	v_fmamk_f32 v58, v58, 0x3a000000, v210
	v_cmp_gt_f32_e32 vcc, s25, v58
	v_mul_f32_e32 v59, 0x4f800000, v58
	s_nop 0
	v_cndmask_b32_e32 v58, v58, v59, vcc
	v_sqrt_f32_e32 v59, v58
	s_nop 0
	v_add_u32_e32 v91, -1, v59
	v_fma_f32 v165, -v91, v59, v58
	v_cmp_ge_f32_e64 s[58:59], 0, v165
	v_add_u32_e32 v165, 1, v59
	s_nop 0
	v_cndmask_b32_e64 v91, v59, v91, s[58:59]
	v_fma_f32 v59, -v165, v59, v58
	v_cmp_lt_f32_e64 s[58:59], 0, v59
	s_nop 1
	v_cndmask_b32_e64 v59, v91, v165, s[58:59]
	v_mul_f32_e32 v91, 0x37800000, v59
	v_cndmask_b32_e32 v59, v59, v91, vcc
	v_cmp_class_f32_e32 vcc, v58, v211
	s_nop 1
	v_cndmask_b32_e32 v58, v59, v58, vcc
	v_div_scale_f32 v59, s[20:21], v58, v58, 1.0
	v_rcp_f32_e32 v91, v59
	s_lshl_b64 s[20:21], s[64:65], 11
	v_fma_f32 v165, -v59, v91, 1.0
	v_fmac_f32_e32 v91, v165, v91
	v_div_scale_f32 v165, vcc, 1.0, v58, 1.0
	v_mul_f32_e32 v166, v165, v91
	v_fma_f32 v167, -v59, v166, v165
	v_fmac_f32_e32 v166, v167, v91
	v_fma_f32 v59, -v59, v166, v165
	v_div_fmas_f32 v59, v59, v91, v166
	v_div_fixup_f32 v91, v59, v58, 1.0
	v_mul_f32_e32 v164, v164, v91
	v_mul_f32_e32 v163, v163, v91
	v_mul_f32_e32 v160, v160, v91
	v_mul_f32_e32 v162, v162, v91
	v_mul_f32_e32 v161, v161, v91
	v_mul_f32_e32 v159, v159, v91
	v_mul_f32_e32 v111, v111, v91
	v_mul_f32_e32 v110, v110, v91
	v_lshl_add_u64 v[58:59], v[86:87], 0, s[20:21]
	v_mul_f32_e32 v109, v109, v91
	v_mul_f32_e32 v108, v108, v91
	v_mul_f32_e32 v107, v107, v91
	v_mul_f32_e32 v106, v106, v91
	v_mul_f32_e32 v105, v105, v91
	v_mul_f32_e32 v104, v104, v91
	v_mul_f32_e32 v103, v103, v91
	v_mul_f32_e32 v102, v102, v91
	v_mul_f32_e32 v101, v101, v91
	v_mul_f32_e32 v100, v100, v91
	v_mul_f32_e32 v99, v99, v91
	v_mul_f32_e32 v98, v98, v91
	v_mul_f32_e32 v97, v97, v91
	v_mul_f32_e32 v96, v96, v91
	v_mul_f32_e32 v95, v95, v91
	v_mul_f32_e32 v94, v94, v91
	v_mul_f32_e32 v67, v67, v91
	v_mul_f32_e32 v65, v65, v91
	v_mul_f32_e32 v64, v64, v91
	v_mul_f32_e32 v63, v63, v91
	v_mul_f32_e32 v62, v62, v91
	v_mul_f32_e32 v61, v61, v91
	v_mul_f32_e32 v60, v60, v91
	v_mul_f32_e32 v0, v0, v91
	s_waitcnt vmcnt(10)
	v_lshlrev_b32_e32 v91, 16, v45
	s_waitcnt vmcnt(28)
	v_fma_f32 v166, v186, v160, v194
	s_waitcnt vmcnt(11)
	v_fma_f32 v164, v182, v164, v190
	v_fma_f32 v165, v183, v163, v191
	v_cvt_pk_bf16_f32 v160, v164, v165
	v_fma_f32 v170, v184, v162, v192
	v_fma_f32 v181, v185, v161, v193
	v_fma_f32 v159, v187, v159, v195
	v_fma_f32 v167, v188, v111, v196
	v_fma_f32 v177, v189, v110, v197
	v_cvt_pk_bf16_f32 v161, v170, v181
	v_cvt_pk_bf16_f32 v162, v166, v159
	v_cvt_pk_bf16_f32 v163, v167, v177
	global_store_dwordx4 v[56:57], v[160:163], off
	v_med3_f32 v111, v164, s19, v229
	v_mov_b32_e32 v110, v1
	v_med3_f32 v160, v165, s19, v229
	v_cvt_pk_fp8_f32 v110, v111, v160
	v_med3_f32 v111, v170, s19, v229
	v_med3_f32 v160, v181, s19, v229
	v_med3_f32 v159, v159, s19, v229
	v_cvt_pk_fp8_f32 v110, v111, v160 op_sel:[0,0,1]
	v_med3_f32 v160, v166, s19, v229
	v_mov_b32_e32 v111, v1
	v_cvt_pk_fp8_f32 v111, v160, v159
	v_med3_f32 v159, v167, s19, v229
	v_med3_f32 v160, v177, s19, v229
	v_cvt_pk_fp8_f32 v111, v159, v160 op_sel:[0,0,1]
	v_lshlrev_b32_e32 v159, 16, v48
	global_store_dwordx2 v[58:59], v[110:111], off
	s_waitcnt vmcnt(26)
	v_fma_f32 v110, v104, v203, v213
	s_waitcnt vmcnt(27)
	v_fma_f32 v109, v109, v198, v206
	v_fma_f32 v108, v108, v199, v207
	v_fma_f32 v107, v107, v200, v208
	v_fma_f32 v175, v106, v201, v209
	v_fma_f32 v106, v105, v202, v212
	v_fma_f32 v111, v103, v204, v214
	v_fma_f32 v171, v102, v205, v215
	v_cvt_pk_bf16_f32 v102, v109, v108
	v_cvt_pk_bf16_f32 v103, v107, v175
	v_cvt_pk_bf16_f32 v104, v106, v110
	v_cvt_pk_bf16_f32 v105, v111, v171
	global_store_dwordx4 v[56:57], v[102:105], off offset:1024
	s_nop 1
	v_med3_f32 v103, v109, s19, v229
	v_med3_f32 v104, v108, s19, v229
	v_mov_b32_e32 v102, v1
	v_cvt_pk_fp8_f32 v102, v103, v104
	v_med3_f32 v103, v107, s19, v229
	v_med3_f32 v104, v175, s19, v229
	v_med3_f32 v105, v110, s19, v229
	v_cvt_pk_fp8_f32 v102, v103, v104 op_sel:[0,0,1]
	v_med3_f32 v104, v106, s19, v229
	v_mov_b32_e32 v103, v1
	v_cvt_pk_fp8_f32 v103, v104, v105
	v_med3_f32 v104, v111, s19, v229
	v_med3_f32 v105, v171, s19, v229
	v_lshlrev_b32_e32 v110, 16, v47
	v_cvt_pk_fp8_f32 v103, v104, v105 op_sel:[0,0,1]
	v_and_b32_e32 v111, 0xffff0000, v47
	global_store_dwordx2 v[58:59], v[102:103], off offset:512
	s_nop 0
	s_waitcnt vmcnt(24)
	v_fma_f32 v163, v94, v223, v243
	s_waitcnt vmcnt(12)
	v_fma_f32 v101, v101, v216, v224
	v_fma_f32 v100, v100, v217, v225
	v_fma_f32 v99, v99, v218, v226
	v_fma_f32 v167, v98, v219, v227
	v_fma_f32 v98, v97, v220, v240
	v_fma_f32 v102, v96, v221, v241
	v_fma_f32 v103, v95, v222, v242
	v_cvt_pk_bf16_f32 v94, v101, v100
	v_cvt_pk_bf16_f32 v95, v99, v167
	v_cvt_pk_bf16_f32 v96, v98, v102
	v_cvt_pk_bf16_f32 v97, v103, v163
	global_store_dwordx4 v[56:57], v[94:97], off offset:2048
	v_and_b32_e32 v160, 0xffff0000, v48
	v_lshlrev_b32_e32 v161, 16, v49
	v_med3_f32 v95, v101, s19, v229
	v_med3_f32 v96, v100, s19, v229
	v_mov_b32_e32 v94, v1
	v_cvt_pk_fp8_f32 v94, v95, v96
	v_med3_f32 v95, v99, s19, v229
	v_med3_f32 v96, v167, s19, v229
	v_med3_f32 v97, v102, s19, v229
	v_cvt_pk_fp8_f32 v94, v95, v96 op_sel:[0,0,1]
	v_med3_f32 v96, v98, s19, v229
	v_mov_b32_e32 v95, v1
	v_cvt_pk_fp8_f32 v95, v96, v97
	v_med3_f32 v96, v103, s19, v229
	v_med3_f32 v97, v163, s19, v229
	v_and_b32_e32 v162, 0xffff0000, v49
	v_cvt_pk_fp8_f32 v95, v96, v97 op_sel:[0,0,1]
	v_add_f32_e32 v47, v161, v162
	v_and_b32_e32 v49, 0xffff0000, v34
	v_lshlrev_b32_e32 v48, 16, v35
	global_store_dwordx2 v[58:59], v[94:95], off offset:1024
	s_nop 0
	s_waitcnt vmcnt(22)
	v_fma_f32 v94, v62, v232, v248
	s_waitcnt vmcnt(15)
	v_fma_f32 v67, v67, v244, v236
	v_fma_f32 v65, v65, v245, v237
	v_fma_f32 v64, v64, v246, v238
	v_fma_f32 v109, v63, v247, v239
	v_fma_f32 v95, v61, v233, v249
	v_fma_f32 v96, v60, v234, v250
	v_fma_f32 v105, v0, v235, v251
	v_cvt_pk_bf16_f32 v60, v67, v65
	v_cvt_pk_bf16_f32 v61, v64, v109
	v_cvt_pk_bf16_f32 v62, v94, v95
	v_cvt_pk_bf16_f32 v63, v96, v105
	global_store_dwordx4 v[56:57], v[60:63], off offset:3072
	v_med3_f32 v0, v67, s19, v229
	v_med3_f32 v57, v65, s19, v229
	v_mov_b32_e32 v56, v1
	v_cvt_pk_fp8_f32 v56, v0, v57
	v_med3_f32 v0, v64, s19, v229
	v_med3_f32 v57, v109, s19, v229
	v_med3_f32 v60, v95, s19, v229
	v_cvt_pk_fp8_f32 v56, v0, v57 op_sel:[0,0,1]
	v_med3_f32 v0, v94, s19, v229
	v_mov_b32_e32 v57, v1
	v_cvt_pk_fp8_f32 v57, v0, v60
	v_med3_f32 v0, v96, s19, v229
	v_med3_f32 v60, v105, s19, v229
	v_lshlrev_b32_e32 v108, 16, v46
	v_cvt_pk_fp8_f32 v57, v0, v60 op_sel:[0,0,1]
	v_and_b32_e32 v109, 0xffff0000, v46
	v_add_f32_e32 v0, v108, v109
	v_add_f32_e32 v46, v110, v111
	v_lshlrev_b32_e32 v99, 16, v42
	v_and_b32_e32 v98, 0xffff0000, v42
	v_lshlrev_b32_e32 v97, 16, v43
	v_and_b32_e32 v96, 0xffff0000, v43
	v_add_f32_e32 v0, v0, v46
	v_add_f32_e32 v46, v159, v160
	v_lshlrev_b32_e32 v95, 16, v44
	v_and_b32_e32 v94, 0xffff0000, v44
	v_and_b32_e32 v67, 0xffff0000, v45
	v_add_f32_e32 v42, v99, v98
	v_add_f32_e32 v43, v97, v96
	v_lshlrev_b32_e32 v65, 16, v38
	v_and_b32_e32 v64, 0xffff0000, v38
	v_lshlrev_b32_e32 v63, 16, v39
	v_and_b32_e32 v62, 0xffff0000, v39
	global_store_dwordx2 v[58:59], v[56:57], off offset:1536
	v_add_f32_e32 v46, v46, v47
	v_add_f32_e32 v42, v42, v43
	v_add_f32_e32 v43, v95, v94
	v_add_f32_e32 v44, v91, v67
	v_lshlrev_b32_e32 v61, 16, v40
	v_and_b32_e32 v60, 0xffff0000, v40
	v_lshlrev_b32_e32 v59, 16, v41
	v_and_b32_e32 v58, 0xffff0000, v41
	v_add_f32_e32 v38, v65, v64
	v_add_f32_e32 v39, v63, v62
	v_add_f32_e32 v0, v0, v46
	v_add_f32_e32 v43, v43, v44
	v_add_f32_e32 v38, v38, v39
	v_add_f32_e32 v39, v61, v60
	v_add_f32_e32 v40, v59, v58
	v_add_f32_e32 v0, 0, v0
	v_add_f32_e32 v42, v42, v43
	v_add_f32_e32 v39, v39, v40
	v_add_f32_e32 v0, v0, v42
	v_add_f32_e32 v38, v38, v39
	v_lshlrev_b32_e32 v56, 16, v34
	v_and_b32_e32 v47, 0xffff0000, v35
	v_add_f32_e32 v38, v0, v38
	v_lshlrev_b32_e32 v46, 16, v36
	v_and_b32_e32 v45, 0xffff0000, v36
	v_lshlrev_b32_e32 v44, 16, v37
	v_and_b32_e32 v0, 0xffff0000, v37
	v_add_f32_e32 v34, v56, v49
	v_add_f32_e32 v35, v48, v47
	v_add_f32_e32 v34, v34, v35
	v_add_f32_e32 v35, v46, v45
	v_add_f32_e32 v36, v44, v0
	v_add_f32_e32 v35, v35, v36
	v_add_f32_e32 v34, v34, v35
	v_add_f32_e32 v34, v38, v34
	s_nop 1
	s_waitcnt lgkmcnt(0)
	v_add_f32_dpp v34, v34, v34 quad_perm:[1,0,3,2] row_mask:0xf bank_mask:0xf
	s_nop 1
	s_waitcnt lgkmcnt(0)
	v_add_f32_dpp v34, v34, v34 quad_perm:[2,3,0,1] row_mask:0xf bank_mask:0xf
	s_nop 1
	s_waitcnt lgkmcnt(0)
	v_add_f32_dpp v34, v34, v34 row_half_mirror row_mask:0xf bank_mask:0xf
	s_nop 1
	s_waitcnt lgkmcnt(0)
	v_add_f32_dpp v34, v34, v34 row_mirror row_mask:0xf bank_mask:0xf
	ds_swizzle_b32 v35, v34 offset:swizzle(SWAP,16)
	s_waitcnt lgkmcnt(0)
	v_add_f32_e32 v34, v34, v35
	v_mov_b32_e32 v35, v34
	s_nop 1
	v_permlane32_swap_b32_e32 v34, v35
	v_add_f32_e32 v34, v34, v35
	v_fmac_f32_e32 v109, 0xba000000, v34
	v_fmac_f32_e32 v108, 0xba000000, v34
	v_mul_f32_e32 v35, v109, v109
	v_fmac_f32_e32 v35, v108, v108
	v_fmac_f32_e32 v110, 0xba000000, v34
	v_fmac_f32_e32 v35, v110, v110
	v_fmac_f32_e32 v111, 0xba000000, v34
	v_fmac_f32_e32 v35, v111, v111
	v_fmac_f32_e32 v159, 0xba000000, v34
	v_fmac_f32_e32 v35, v159, v159
	v_fmac_f32_e32 v160, 0xba000000, v34
	v_fmac_f32_e32 v35, v160, v160
	v_fmac_f32_e32 v161, 0xba000000, v34
	v_fmac_f32_e32 v35, v161, v161
	v_fmac_f32_e32 v162, 0xba000000, v34
	v_fmac_f32_e32 v35, v162, v162
	v_fmac_f32_e32 v99, 0xba000000, v34
	v_fmac_f32_e32 v35, v99, v99
	v_fmac_f32_e32 v98, 0xba000000, v34
	v_fmac_f32_e32 v35, v98, v98
	v_fmac_f32_e32 v97, 0xba000000, v34
	v_fmac_f32_e32 v35, v97, v97
	v_fmac_f32_e32 v96, 0xba000000, v34
	v_fmac_f32_e32 v35, v96, v96
	v_fmac_f32_e32 v95, 0xba000000, v34
	v_fmac_f32_e32 v35, v95, v95
	v_fmac_f32_e32 v94, 0xba000000, v34
	v_fmac_f32_e32 v35, v94, v94
	v_fmac_f32_e32 v91, 0xba000000, v34
	v_fmac_f32_e32 v35, v91, v91
	v_fmac_f32_e32 v67, 0xba000000, v34
	v_fmac_f32_e32 v35, v67, v67
	v_fmac_f32_e32 v65, 0xba000000, v34
	v_fmac_f32_e32 v35, v65, v65
	v_fmac_f32_e32 v64, 0xba000000, v34
	v_fmac_f32_e32 v35, v64, v64
	v_fmac_f32_e32 v63, 0xba000000, v34
	v_fmac_f32_e32 v35, v63, v63
	v_fmac_f32_e32 v62, 0xba000000, v34
	v_fmac_f32_e32 v35, v62, v62
	v_fmac_f32_e32 v61, 0xba000000, v34
	v_fmac_f32_e32 v35, v61, v61
	v_fmac_f32_e32 v60, 0xba000000, v34
	v_fmac_f32_e32 v35, v60, v60
	v_fmac_f32_e32 v59, 0xba000000, v34
	v_fmac_f32_e32 v35, v59, v59
	v_fmac_f32_e32 v58, 0xba000000, v34
	v_fmac_f32_e32 v35, v58, v58
	v_fmac_f32_e32 v56, 0xba000000, v34
	v_fmac_f32_e32 v35, v56, v56
	v_fmac_f32_e32 v49, 0xba000000, v34
	v_fmac_f32_e32 v35, v49, v49
	v_fmac_f32_e32 v48, 0xba000000, v34
	v_fmac_f32_e32 v35, v48, v48
	v_fmac_f32_e32 v47, 0xba000000, v34
	v_fmac_f32_e32 v35, v47, v47
	v_fmac_f32_e32 v46, 0xba000000, v34
	v_fmac_f32_e32 v35, v46, v46
	v_fmac_f32_e32 v45, 0xba000000, v34
	v_fmac_f32_e32 v35, v45, v45
	v_fmac_f32_e32 v44, 0xba000000, v34
	v_fmac_f32_e32 v35, v44, v44
	v_fmac_f32_e32 v0, 0xba000000, v34
	v_fmac_f32_e32 v35, v0, v0
	s_nop 1
	s_waitcnt lgkmcnt(0)
	v_add_f32_dpp v34, v35, v35 quad_perm:[1,0,3,2] row_mask:0xf bank_mask:0xf
	s_nop 1
	s_waitcnt lgkmcnt(0)
	v_add_f32_dpp v34, v34, v34 quad_perm:[2,3,0,1] row_mask:0xf bank_mask:0xf
	s_nop 1
	s_waitcnt lgkmcnt(0)
	v_add_f32_dpp v34, v34, v34 row_half_mirror row_mask:0xf bank_mask:0xf
	s_nop 1
	s_waitcnt lgkmcnt(0)
	v_add_f32_dpp v34, v34, v34 row_mirror row_mask:0xf bank_mask:0xf
	ds_swizzle_b32 v35, v34 offset:swizzle(SWAP,16)
	s_waitcnt lgkmcnt(0)
	v_add_f32_e32 v34, v34, v35
	v_mov_b32_e32 v35, v34
	s_nop 1
	v_permlane32_swap_b32_e32 v34, v35
	v_add_f32_e32 v34, v34, v35
	v_fmamk_f32 v34, v34, 0x3a000000, v210
	v_cmp_gt_f32_e32 vcc, s25, v34
	v_mul_f32_e32 v35, 0x4f800000, v34
	s_nop 0
	v_cndmask_b32_e32 v34, v34, v35, vcc
	v_sqrt_f32_e32 v35, v34
	s_nop 0
	v_add_u32_e32 v36, -1, v35
	v_fma_f32 v37, -v36, v35, v34
	v_cmp_ge_f32_e64 s[58:59], 0, v37
	v_add_u32_e32 v37, 1, v35
	s_nop 0
	v_cndmask_b32_e64 v36, v35, v36, s[58:59]
	v_fma_f32 v35, -v37, v35, v34
	v_cmp_lt_f32_e64 s[58:59], 0, v35
	s_nop 1
	v_cndmask_b32_e64 v35, v36, v37, s[58:59]
	v_mul_f32_e32 v36, 0x37800000, v35
	v_cndmask_b32_e32 v35, v35, v36, vcc
	v_cmp_class_f32_e32 vcc, v34, v211
	s_nop 1
	v_cndmask_b32_e32 v34, v35, v34, vcc
	v_div_scale_f32 v35, s[20:21], v34, v34, 1.0
	v_rcp_f32_e32 v36, v35
	s_lshl_b64 s[20:21], s[62:63], 11
	v_lshl_add_u64 v[42:43], v[86:87], 0, s[20:21]
	v_fma_f32 v37, -v35, v36, 1.0
	v_fmac_f32_e32 v36, v37, v36
	v_div_scale_f32 v37, vcc, 1.0, v34, 1.0
	v_mul_f32_e32 v38, v37, v36
	v_fma_f32 v39, -v35, v38, v37
	v_fmac_f32_e32 v38, v39, v36
	v_fma_f32 v35, -v35, v38, v37
	v_div_fmas_f32 v35, v35, v36, v38
	v_div_fixup_f32 v57, v35, v34, 1.0
	v_mul_f32_e32 v108, v108, v57
	v_mul_f32_e32 v96, v96, v57
	v_mul_f32_e32 v99, v99, v57
	v_mul_f32_e32 v98, v98, v57
	v_mul_f32_e32 v97, v97, v57
	v_mul_f32_e32 v62, v62, v57
	v_mul_f32_e32 v65, v65, v57
	v_mul_f32_e32 v64, v64, v57
	v_mul_f32_e32 v63, v63, v57
	v_mul_f32_e32 v47, v47, v57
	v_mul_f32_e32 v56, v56, v57
	v_mul_f32_e32 v49, v49, v57
	v_mul_f32_e32 v48, v48, v57
	v_mul_f32_e32 v0, v0, v57
	s_waitcnt vmcnt(63)
	v_fma_f32 v104, v182, v108, v190
	v_mul_f32_e32 v38, v109, v57
	v_fma_f32 v105, v183, v38, v191
	v_mul_f32_e32 v39, v111, v57
	v_fma_f32 v41, v185, v39, v193
	v_mul_f32_e32 v39, v159, v57
	v_fma_f32 v39, v186, v39, v194
	v_mul_f32_e32 v34, v160, v57
	v_fma_f32 v35, v187, v34, v195
	v_mul_f32_e32 v34, v161, v57
	v_mul_f32_e32 v38, v110, v57
	v_fma_f32 v34, v188, v34, v196
	v_mul_f32_e32 v36, v162, v57
	v_cvt_pk_bf16_f32 v100, v104, v105
	v_fma_f32 v38, v184, v38, v192
	v_fma_f32 v37, v189, v36, v197
	v_cvt_pk_bf16_f32 v101, v38, v41
	v_cvt_pk_bf16_f32 v102, v39, v35
	v_cvt_pk_bf16_f32 v103, v34, v37
	global_store_dwordx4 v[54:55], v[100:103], off
	v_med3_f32 v36, v104, s19, v229
	v_med3_f32 v40, v105, s19, v229
	v_mov_b32_e32 v100, v1
	v_cvt_pk_fp8_f32 v100, v36, v40
	v_med3_f32 v36, v38, s19, v229
	v_med3_f32 v38, v41, s19, v229
	v_med3_f32 v35, v35, s19, v229
	v_cvt_pk_fp8_f32 v100, v36, v38 op_sel:[0,0,1]
	v_med3_f32 v36, v39, s19, v229
	v_mov_b32_e32 v101, v1
	v_cvt_pk_fp8_f32 v101, v36, v35
	v_med3_f32 v34, v34, s19, v229
	v_med3_f32 v35, v37, s19, v229
	v_cvt_pk_fp8_f32 v101, v34, v35 op_sel:[0,0,1]
	global_store_dwordx2 v[42:43], v[100:101], off
	s_nop 0
	s_waitcnt vmcnt(17)
	v_fma_f32 v107, v96, v201, v209
	v_mul_f32_e32 v41, v95, v57
	v_fma_f32 v41, v41, v202, v212
	v_mul_f32_e32 v34, v94, v57
	v_fma_f32 v94, v34, v203, v213
	v_mul_f32_e32 v34, v91, v57
	v_fma_f32 v91, v34, v204, v214
	v_mul_f32_e32 v34, v67, v57
	v_fma_f32 v38, v99, v198, v206
	v_fma_f32 v39, v98, v199, v207
	v_fma_f32 v40, v97, v200, v208
	v_fma_f32 v103, v34, v205, v215
	v_cvt_pk_bf16_f32 v34, v38, v39
	v_cvt_pk_bf16_f32 v35, v40, v107
	v_cvt_pk_bf16_f32 v36, v41, v94
	v_cvt_pk_bf16_f32 v37, v91, v103
	global_store_dwordx4 v[54:55], v[34:37], off offset:1024
	v_lshlrev_b32_e32 v67, 16, v31
	s_nop 0
	v_med3_f32 v35, v38, s19, v229
	v_med3_f32 v36, v39, s19, v229
	v_mov_b32_e32 v34, v1
	v_cvt_pk_fp8_f32 v34, v35, v36
	v_med3_f32 v35, v40, s19, v229
	v_med3_f32 v36, v107, s19, v229
	v_med3_f32 v37, v94, s19, v229
	v_cvt_pk_fp8_f32 v34, v35, v36 op_sel:[0,0,1]
	v_med3_f32 v36, v41, s19, v229
	v_mov_b32_e32 v35, v1
	v_cvt_pk_fp8_f32 v35, v36, v37
	v_med3_f32 v36, v91, s19, v229
	v_med3_f32 v37, v103, s19, v229
	v_and_b32_e32 v91, 0xffff0000, v31
	v_cvt_pk_fp8_f32 v35, v36, v37 op_sel:[0,0,1]
	global_store_dwordx2 v[42:43], v[34:35], off offset:512
	s_nop 0
	s_waitcnt vmcnt(16)
	v_fma_f32 v101, v62, v219, v227
	v_mul_f32_e32 v41, v61, v57
	v_fma_f32 v41, v41, v220, v240
	v_mul_f32_e32 v34, v60, v57
	v_fma_f32 v60, v34, v221, v241
	v_mul_f32_e32 v34, v59, v57
	v_fma_f32 v59, v34, v222, v242
	v_mul_f32_e32 v34, v58, v57
	v_fma_f32 v38, v65, v216, v224
	v_fma_f32 v39, v64, v217, v225
	v_fma_f32 v40, v63, v218, v226
	v_fma_f32 v97, v34, v223, v243
	v_cvt_pk_bf16_f32 v34, v38, v39
	v_cvt_pk_bf16_f32 v35, v40, v101
	v_cvt_pk_bf16_f32 v36, v41, v60
	v_cvt_pk_bf16_f32 v37, v59, v97
	global_store_dwordx4 v[54:55], v[34:37], off offset:2048
	v_lshlrev_b32_e32 v94, 16, v32
	v_and_b32_e32 v95, 0xffff0000, v32
	v_med3_f32 v35, v38, s19, v229
	v_med3_f32 v36, v39, s19, v229
	v_mov_b32_e32 v34, v1
	v_cvt_pk_fp8_f32 v34, v35, v36
	v_med3_f32 v35, v40, s19, v229
	v_med3_f32 v36, v101, s19, v229
	v_med3_f32 v37, v60, s19, v229
	v_cvt_pk_fp8_f32 v34, v35, v36 op_sel:[0,0,1]
	v_med3_f32 v36, v41, s19, v229
	v_mov_b32_e32 v35, v1
	v_cvt_pk_fp8_f32 v35, v36, v37
	v_med3_f32 v36, v59, s19, v229
	v_med3_f32 v37, v97, s19, v229
	v_lshlrev_b32_e32 v96, 16, v33
	v_cvt_pk_fp8_f32 v35, v36, v37 op_sel:[0,0,1]
	v_and_b32_e32 v97, 0xffff0000, v33
	v_add_f32_e32 v31, v96, v97
	v_and_b32_e32 v33, 0xffff0000, v18
	global_store_dwordx2 v[42:43], v[34:35], off offset:1024
	s_nop 0
	v_lshlrev_b32_e32 v32, 16, v19
	s_waitcnt vmcnt(63)
	v_fma_f32 v61, v0, v235, v251
	s_waitcnt vmcnt(19)
	v_fma_f32 v65, v47, v247, v239
	v_mul_f32_e32 v41, v46, v57
	v_fma_f32 v41, v41, v232, v248
	v_mul_f32_e32 v34, v45, v57
	v_fma_f32 v45, v34, v233, v249
	v_mul_f32_e32 v34, v44, v57
	v_fma_f32 v38, v56, v244, v236
	v_fma_f32 v39, v49, v245, v237
	v_fma_f32 v40, v48, v246, v238
	v_fma_f32 v44, v34, v234, v250
	v_cvt_pk_bf16_f32 v34, v38, v39
	v_cvt_pk_bf16_f32 v35, v40, v65
	v_cvt_pk_bf16_f32 v36, v41, v45
	v_cvt_pk_bf16_f32 v37, v44, v61
	global_store_dwordx4 v[54:55], v[34:37], off offset:3072
	v_med3_f32 v0, v38, s19, v229
	v_lshlrev_b32_e32 v64, 16, v30
	v_med3_f32 v35, v39, s19, v229
	v_mov_b32_e32 v34, v1
	v_cvt_pk_fp8_f32 v34, v0, v35
	v_med3_f32 v0, v40, s19, v229
	v_med3_f32 v35, v65, s19, v229
	v_med3_f32 v36, v45, s19, v229
	v_cvt_pk_fp8_f32 v34, v0, v35 op_sel:[0,0,1]
	v_med3_f32 v0, v41, s19, v229
	v_mov_b32_e32 v35, v1
	v_cvt_pk_fp8_f32 v35, v0, v36
	v_med3_f32 v0, v44, s19, v229
	v_med3_f32 v36, v61, s19, v229
	v_and_b32_e32 v65, 0xffff0000, v30
	v_cvt_pk_fp8_f32 v35, v0, v36 op_sel:[0,0,1]
	v_add_f32_e32 v0, v64, v65
	v_add_f32_e32 v30, v67, v91
	v_lshlrev_b32_e32 v55, 16, v26
	v_and_b32_e32 v54, 0xffff0000, v26
	v_lshlrev_b32_e32 v49, 16, v27
	v_and_b32_e32 v48, 0xffff0000, v27
	global_store_dwordx2 v[42:43], v[34:35], off offset:1536
	v_add_f32_e32 v0, v0, v30
	v_add_f32_e32 v30, v94, v95
	v_lshlrev_b32_e32 v47, 16, v28
	v_and_b32_e32 v46, 0xffff0000, v28
	v_lshlrev_b32_e32 v45, 16, v29
	v_and_b32_e32 v44, 0xffff0000, v29
	v_add_f32_e32 v26, v55, v54
	v_add_f32_e32 v27, v49, v48
	v_lshlrev_b32_e32 v43, 16, v22
	v_and_b32_e32 v42, 0xffff0000, v22
	v_lshlrev_b32_e32 v41, 16, v23
	v_and_b32_e32 v40, 0xffff0000, v23
	v_add_f32_e32 v30, v30, v31
	v_add_f32_e32 v26, v26, v27
	v_add_f32_e32 v27, v47, v46
	v_add_f32_e32 v28, v45, v44
	v_lshlrev_b32_e32 v39, 16, v24
	v_and_b32_e32 v38, 0xffff0000, v24
	v_lshlrev_b32_e32 v37, 16, v25
	v_and_b32_e32 v36, 0xffff0000, v25
	v_add_f32_e32 v22, v43, v42
	v_add_f32_e32 v23, v41, v40
	v_add_f32_e32 v0, v0, v30
	v_add_f32_e32 v27, v27, v28
	v_add_f32_e32 v22, v22, v23
	v_add_f32_e32 v23, v39, v38
	v_add_f32_e32 v24, v37, v36
	v_add_f32_e32 v0, 0, v0
	v_add_f32_e32 v26, v26, v27
	v_add_f32_e32 v23, v23, v24
	v_add_f32_e32 v0, v0, v26
	v_add_f32_e32 v22, v22, v23
	v_lshlrev_b32_e32 v34, 16, v18
	v_and_b32_e32 v31, 0xffff0000, v19
	v_add_f32_e32 v22, v0, v22
	v_lshlrev_b32_e32 v30, 16, v20
	v_and_b32_e32 v29, 0xffff0000, v20
	v_lshlrev_b32_e32 v28, 16, v21
	v_and_b32_e32 v0, 0xffff0000, v21
	v_add_f32_e32 v18, v34, v33
	v_add_f32_e32 v19, v32, v31
	v_add_f32_e32 v18, v18, v19
	v_add_f32_e32 v19, v30, v29
	v_add_f32_e32 v20, v28, v0
	v_add_f32_e32 v19, v19, v20
	v_add_f32_e32 v18, v18, v19
	v_add_f32_e32 v18, v22, v18
	s_nop 1
	s_waitcnt lgkmcnt(0)
	v_add_f32_dpp v18, v18, v18 quad_perm:[1,0,3,2] row_mask:0xf bank_mask:0xf
	s_nop 1
	s_waitcnt lgkmcnt(0)
	v_add_f32_dpp v18, v18, v18 quad_perm:[2,3,0,1] row_mask:0xf bank_mask:0xf
	s_nop 1
	s_waitcnt lgkmcnt(0)
	v_add_f32_dpp v18, v18, v18 row_half_mirror row_mask:0xf bank_mask:0xf
	s_nop 1
	s_waitcnt lgkmcnt(0)
	v_add_f32_dpp v18, v18, v18 row_mirror row_mask:0xf bank_mask:0xf
	ds_swizzle_b32 v19, v18 offset:swizzle(SWAP,16)
	s_waitcnt lgkmcnt(0)
	v_add_f32_e32 v18, v18, v19
	v_mov_b32_e32 v19, v18
	s_nop 1
	v_permlane32_swap_b32_e32 v18, v19
	v_add_f32_e32 v18, v18, v19
	v_fmac_f32_e32 v65, 0xba000000, v18
	v_fmac_f32_e32 v64, 0xba000000, v18
	v_mul_f32_e32 v19, v65, v65
	v_fmac_f32_e32 v19, v64, v64
	v_fmac_f32_e32 v67, 0xba000000, v18
	v_fmac_f32_e32 v19, v67, v67
	v_fmac_f32_e32 v91, 0xba000000, v18
	v_fmac_f32_e32 v19, v91, v91
	v_fmac_f32_e32 v94, 0xba000000, v18
	v_fmac_f32_e32 v19, v94, v94
	v_fmac_f32_e32 v95, 0xba000000, v18
	v_fmac_f32_e32 v19, v95, v95
	v_fmac_f32_e32 v96, 0xba000000, v18
	v_fmac_f32_e32 v19, v96, v96
	v_fmac_f32_e32 v97, 0xba000000, v18
	v_fmac_f32_e32 v19, v97, v97
	v_fmac_f32_e32 v55, 0xba000000, v18
	v_fmac_f32_e32 v19, v55, v55
	v_fmac_f32_e32 v54, 0xba000000, v18
	v_fmac_f32_e32 v19, v54, v54
	v_fmac_f32_e32 v49, 0xba000000, v18
	v_fmac_f32_e32 v19, v49, v49
	v_fmac_f32_e32 v48, 0xba000000, v18
	v_fmac_f32_e32 v19, v48, v48
	v_fmac_f32_e32 v47, 0xba000000, v18
	v_fmac_f32_e32 v19, v47, v47
	v_fmac_f32_e32 v46, 0xba000000, v18
	v_fmac_f32_e32 v19, v46, v46
	v_fmac_f32_e32 v45, 0xba000000, v18
	v_fmac_f32_e32 v19, v45, v45
	v_fmac_f32_e32 v44, 0xba000000, v18
	v_fmac_f32_e32 v19, v44, v44
	v_fmac_f32_e32 v43, 0xba000000, v18
	v_fmac_f32_e32 v19, v43, v43
	v_fmac_f32_e32 v42, 0xba000000, v18
	v_fmac_f32_e32 v19, v42, v42
	v_fmac_f32_e32 v41, 0xba000000, v18
	v_fmac_f32_e32 v19, v41, v41
	v_fmac_f32_e32 v40, 0xba000000, v18
	v_fmac_f32_e32 v19, v40, v40
	v_fmac_f32_e32 v39, 0xba000000, v18
	v_fmac_f32_e32 v19, v39, v39
	v_fmac_f32_e32 v38, 0xba000000, v18
	v_fmac_f32_e32 v19, v38, v38
	v_fmac_f32_e32 v37, 0xba000000, v18
	v_fmac_f32_e32 v19, v37, v37
	v_fmac_f32_e32 v36, 0xba000000, v18
	v_fmac_f32_e32 v19, v36, v36
	v_fmac_f32_e32 v34, 0xba000000, v18
	v_fmac_f32_e32 v19, v34, v34
	v_fmac_f32_e32 v33, 0xba000000, v18
	v_fmac_f32_e32 v19, v33, v33
	v_fmac_f32_e32 v32, 0xba000000, v18
	v_fmac_f32_e32 v19, v32, v32
	v_fmac_f32_e32 v31, 0xba000000, v18
	v_fmac_f32_e32 v19, v31, v31
	v_fmac_f32_e32 v30, 0xba000000, v18
	v_fmac_f32_e32 v19, v30, v30
	v_fmac_f32_e32 v29, 0xba000000, v18
	v_fmac_f32_e32 v19, v29, v29
	v_fmac_f32_e32 v28, 0xba000000, v18
	v_fmac_f32_e32 v19, v28, v28
	v_fmac_f32_e32 v0, 0xba000000, v18
	v_fmac_f32_e32 v19, v0, v0
	s_nop 1
	s_waitcnt lgkmcnt(0)
	v_add_f32_dpp v18, v19, v19 quad_perm:[1,0,3,2] row_mask:0xf bank_mask:0xf
	s_nop 1
	s_waitcnt lgkmcnt(0)
	v_add_f32_dpp v18, v18, v18 quad_perm:[2,3,0,1] row_mask:0xf bank_mask:0xf
	s_nop 1
	s_waitcnt lgkmcnt(0)
	v_add_f32_dpp v18, v18, v18 row_half_mirror row_mask:0xf bank_mask:0xf
	s_nop 1
	s_waitcnt lgkmcnt(0)
	v_add_f32_dpp v18, v18, v18 row_mirror row_mask:0xf bank_mask:0xf
	ds_swizzle_b32 v19, v18 offset:swizzle(SWAP,16)
	s_waitcnt lgkmcnt(0)
	v_add_f32_e32 v18, v18, v19
	v_mov_b32_e32 v19, v18
	s_nop 1
	v_permlane32_swap_b32_e32 v18, v19
	v_add_f32_e32 v18, v18, v19
	v_fmamk_f32 v18, v18, 0x3a000000, v210
	v_cmp_gt_f32_e32 vcc, s25, v18
	v_mul_f32_e32 v19, 0x4f800000, v18
	s_nop 0
	v_cndmask_b32_e32 v18, v18, v19, vcc
	v_sqrt_f32_e32 v19, v18
	s_nop 0
	v_add_u32_e32 v20, -1, v19
	v_fma_f32 v21, -v20, v19, v18
	v_cmp_ge_f32_e64 s[58:59], 0, v21
	v_add_u32_e32 v21, 1, v19
	s_nop 0
	v_cndmask_b32_e64 v20, v19, v20, s[58:59]
	v_fma_f32 v19, -v21, v19, v18
	v_cmp_lt_f32_e64 s[58:59], 0, v19
	s_nop 1
	v_cndmask_b32_e64 v19, v20, v21, s[58:59]
	v_mul_f32_e32 v20, 0x37800000, v19
	v_cndmask_b32_e32 v19, v19, v20, vcc
	v_cmp_class_f32_e32 vcc, v18, v211
	s_nop 1
	v_cndmask_b32_e32 v18, v19, v18, vcc
	v_div_scale_f32 v19, s[20:21], v18, v18, 1.0
	v_rcp_f32_e32 v20, v19
	s_lshl_b64 s[20:21], s[60:61], 11
	v_lshl_add_u64 v[26:27], v[86:87], 0, s[20:21]
	v_fma_f32 v21, -v19, v20, 1.0
	v_fmac_f32_e32 v20, v21, v20
	v_div_scale_f32 v21, vcc, 1.0, v18, 1.0
	v_mul_f32_e32 v22, v21, v20
	v_fma_f32 v23, -v19, v22, v21
	v_fmac_f32_e32 v22, v23, v20
	v_fma_f32 v19, -v19, v22, v21
	v_div_fmas_f32 v19, v19, v20, v22
	v_div_fixup_f32 v35, v19, v18, 1.0
	v_mul_f32_e32 v64, v64, v35
	v_mul_f32_e32 v48, v48, v35
	v_mul_f32_e32 v55, v55, v35
	v_mul_f32_e32 v54, v54, v35
	v_mul_f32_e32 v49, v49, v35
	v_mul_f32_e32 v40, v40, v35
	v_mul_f32_e32 v43, v43, v35
	v_mul_f32_e32 v42, v42, v35
	v_mul_f32_e32 v41, v41, v35
	v_mul_f32_e32 v31, v31, v35
	v_mul_f32_e32 v34, v34, v35
	v_mul_f32_e32 v33, v33, v35
	v_mul_f32_e32 v32, v32, v35
	v_mul_f32_e32 v0, v0, v35
	s_waitcnt vmcnt(63)
	v_fma_f32 v60, v182, v64, v190
	v_mul_f32_e32 v22, v65, v35
	v_fma_f32 v61, v183, v22, v191
	v_mul_f32_e32 v23, v91, v35
	v_fma_f32 v25, v185, v23, v193
	v_mul_f32_e32 v23, v94, v35
	v_fma_f32 v23, v186, v23, v194
	v_mul_f32_e32 v18, v95, v35
	v_fma_f32 v19, v187, v18, v195
	v_mul_f32_e32 v18, v96, v35
	v_mul_f32_e32 v22, v67, v35
	v_fma_f32 v18, v188, v18, v196
	v_mul_f32_e32 v20, v97, v35
	v_cvt_pk_bf16_f32 v56, v60, v61
	v_fma_f32 v22, v184, v22, v192
	v_fma_f32 v21, v189, v20, v197
	v_cvt_pk_bf16_f32 v57, v22, v25
	v_cvt_pk_bf16_f32 v58, v23, v19
	v_cvt_pk_bf16_f32 v59, v18, v21
	global_store_dwordx4 v[52:53], v[56:59], off
	v_med3_f32 v20, v60, s19, v229
	v_med3_f32 v24, v61, s19, v229
	v_mov_b32_e32 v56, v1
	v_cvt_pk_fp8_f32 v56, v20, v24
	v_med3_f32 v20, v22, s19, v229
	v_med3_f32 v22, v25, s19, v229
	v_med3_f32 v19, v19, s19, v229
	v_cvt_pk_fp8_f32 v56, v20, v22 op_sel:[0,0,1]
	v_med3_f32 v20, v23, s19, v229
	v_mov_b32_e32 v57, v1
	v_cvt_pk_fp8_f32 v57, v20, v19
	v_med3_f32 v18, v18, s19, v229
	v_med3_f32 v19, v21, s19, v229
	v_cvt_pk_fp8_f32 v57, v18, v19 op_sel:[0,0,1]
	global_store_dwordx2 v[26:27], v[56:57], off
	s_nop 0
	s_waitcnt vmcnt(18)
	v_fma_f32 v63, v48, v201, v209
	v_mul_f32_e32 v25, v47, v35
	v_fma_f32 v25, v25, v202, v212
	v_mul_f32_e32 v18, v46, v35
	v_fma_f32 v46, v18, v203, v213
	v_mul_f32_e32 v18, v45, v35
	v_fma_f32 v45, v18, v204, v214
	v_mul_f32_e32 v18, v44, v35
	v_fma_f32 v22, v55, v198, v206
	v_fma_f32 v23, v54, v199, v207
	v_fma_f32 v24, v49, v200, v208
	v_fma_f32 v59, v18, v205, v215
	v_cvt_pk_bf16_f32 v18, v22, v23
	v_cvt_pk_bf16_f32 v19, v24, v63
	v_cvt_pk_bf16_f32 v20, v25, v46
	v_cvt_pk_bf16_f32 v21, v45, v59
	global_store_dwordx4 v[52:53], v[18:21], off offset:1024
	v_lshlrev_b32_e32 v48, 16, v16
	v_and_b32_e32 v49, 0xffff0000, v16
	v_med3_f32 v19, v22, s19, v229
	v_med3_f32 v20, v23, s19, v229
	v_mov_b32_e32 v18, v1
	v_cvt_pk_fp8_f32 v18, v19, v20
	v_med3_f32 v19, v24, s19, v229
	v_med3_f32 v20, v63, s19, v229
	v_med3_f32 v21, v46, s19, v229
	v_cvt_pk_fp8_f32 v18, v19, v20 op_sel:[0,0,1]
	v_med3_f32 v20, v25, s19, v229
	v_mov_b32_e32 v19, v1
	v_cvt_pk_fp8_f32 v19, v20, v21
	v_med3_f32 v20, v45, s19, v229
	v_med3_f32 v21, v59, s19, v229
	v_lshlrev_b32_e32 v16, 16, v3
	v_cvt_pk_fp8_f32 v19, v20, v21 op_sel:[0,0,1]
	global_store_dwordx2 v[26:27], v[18:19], off offset:512
	s_nop 0
	s_waitcnt vmcnt(63)
	v_fma_f32 v57, v40, v219, v227
	v_mul_f32_e32 v25, v39, v35
	v_fma_f32 v25, v25, v220, v240
	v_mul_f32_e32 v18, v38, v35
	v_fma_f32 v38, v18, v221, v241
	v_mul_f32_e32 v18, v37, v35
	v_fma_f32 v37, v18, v222, v242
	v_mul_f32_e32 v18, v36, v35
	v_fma_f32 v22, v43, v216, v224
	v_fma_f32 v23, v42, v217, v225
	v_fma_f32 v24, v41, v218, v226
	v_fma_f32 v47, v18, v223, v243
	v_cvt_pk_bf16_f32 v18, v22, v23
	v_cvt_pk_bf16_f32 v19, v24, v57
	v_cvt_pk_bf16_f32 v20, v25, v38
	v_cvt_pk_bf16_f32 v21, v37, v47
	global_store_dwordx4 v[52:53], v[18:21], off offset:2048
	v_lshlrev_b32_e32 v44, 16, v14
	v_and_b32_e32 v45, 0xffff0000, v14
	v_med3_f32 v19, v22, s19, v229
	v_med3_f32 v20, v23, s19, v229
	v_mov_b32_e32 v18, v1
	v_cvt_pk_fp8_f32 v18, v19, v20
	v_med3_f32 v19, v24, s19, v229
	v_med3_f32 v20, v57, s19, v229
	v_med3_f32 v21, v38, s19, v229
	v_cvt_pk_fp8_f32 v18, v19, v20 op_sel:[0,0,1]
	v_med3_f32 v20, v25, s19, v229
	v_mov_b32_e32 v19, v1
	v_cvt_pk_fp8_f32 v19, v20, v21
	v_med3_f32 v20, v37, s19, v229
	v_med3_f32 v21, v47, s19, v229
	v_lshlrev_b32_e32 v46, 16, v15
	v_cvt_pk_fp8_f32 v19, v20, v21 op_sel:[0,0,1]
	v_and_b32_e32 v47, 0xffff0000, v15
	v_add_f32_e32 v14, v46, v47
	global_store_dwordx2 v[26:27], v[18:19], off offset:1024
	s_nop 0
	s_waitcnt vmcnt(63)
	v_fma_f32 v39, v0, v235, v251
	s_waitcnt vmcnt(23)
	v_fma_f32 v43, v31, v247, v239
	v_mul_f32_e32 v25, v30, v35
	v_fma_f32 v25, v25, v232, v248
	v_mul_f32_e32 v18, v29, v35
	v_fma_f32 v29, v18, v233, v249
	v_mul_f32_e32 v18, v28, v35
	v_fma_f32 v22, v34, v244, v236
	v_fma_f32 v23, v33, v245, v237
	v_fma_f32 v24, v32, v246, v238
	v_fma_f32 v28, v18, v234, v250
	v_cvt_pk_bf16_f32 v18, v22, v23
	v_cvt_pk_bf16_f32 v19, v24, v43
	v_cvt_pk_bf16_f32 v20, v25, v29
	v_cvt_pk_bf16_f32 v21, v28, v39
	global_store_dwordx4 v[52:53], v[18:21], off offset:3072
	v_med3_f32 v0, v22, s19, v229
	v_lshlrev_b32_e32 v52, 16, v17
	v_med3_f32 v19, v23, s19, v229
	v_mov_b32_e32 v18, v1
	v_cvt_pk_fp8_f32 v18, v0, v19
	v_med3_f32 v0, v24, s19, v229
	v_med3_f32 v19, v43, s19, v229
	v_med3_f32 v20, v29, s19, v229
	v_cvt_pk_fp8_f32 v18, v0, v19 op_sel:[0,0,1]
	v_med3_f32 v0, v25, s19, v229
	v_mov_b32_e32 v19, v1
	v_cvt_pk_fp8_f32 v19, v0, v20
	v_med3_f32 v0, v28, s19, v229
	v_med3_f32 v20, v39, s19, v229
	v_and_b32_e32 v53, 0xffff0000, v17
	v_cvt_pk_fp8_f32 v19, v0, v20 op_sel:[0,0,1]
	v_add_f32_e32 v0, v44, v45
	v_lshlrev_b32_e32 v35, 16, v10
	v_and_b32_e32 v34, 0xffff0000, v10
	v_lshlrev_b32_e32 v33, 16, v11
	v_and_b32_e32 v32, 0xffff0000, v11
	global_store_dwordx2 v[26:27], v[18:19], off offset:1536
	v_add_f32_e32 v0, v0, v14
	v_add_f32_e32 v14, v48, v49
	v_add_f32_e32 v15, v52, v53
	v_lshlrev_b32_e32 v31, 16, v12
	v_and_b32_e32 v30, 0xffff0000, v12
	v_lshlrev_b32_e32 v29, 16, v13
	v_and_b32_e32 v28, 0xffff0000, v13
	v_add_f32_e32 v10, v35, v34
	v_add_f32_e32 v11, v33, v32
	v_lshlrev_b32_e32 v27, 16, v6
	v_and_b32_e32 v26, 0xffff0000, v6
	v_lshlrev_b32_e32 v25, 16, v7
	v_and_b32_e32 v24, 0xffff0000, v7
	v_add_f32_e32 v14, v14, v15
	v_add_f32_e32 v10, v10, v11
	v_add_f32_e32 v11, v31, v30
	v_add_f32_e32 v12, v29, v28
	v_lshlrev_b32_e32 v23, 16, v8
	v_and_b32_e32 v22, 0xffff0000, v8
	v_lshlrev_b32_e32 v21, 16, v9
	v_and_b32_e32 v20, 0xffff0000, v9
	v_add_f32_e32 v6, v27, v26
	v_add_f32_e32 v7, v25, v24
	v_add_f32_e32 v0, v0, v14
	v_add_f32_e32 v11, v11, v12
	v_add_f32_e32 v6, v6, v7
	v_add_f32_e32 v7, v23, v22
	v_add_f32_e32 v8, v21, v20
	v_add_f32_e32 v0, 0, v0
	v_add_f32_e32 v10, v10, v11
	v_add_f32_e32 v7, v7, v8
	v_add_f32_e32 v0, v0, v10
	v_add_f32_e32 v6, v6, v7
	v_lshlrev_b32_e32 v18, 16, v2
	v_and_b32_e32 v17, 0xffff0000, v2
	v_and_b32_e32 v15, 0xffff0000, v3
	v_add_f32_e32 v6, v0, v6
	v_lshlrev_b32_e32 v14, 16, v4
	v_and_b32_e32 v13, 0xffff0000, v4
	v_lshlrev_b32_e32 v12, 16, v5
	v_and_b32_e32 v0, 0xffff0000, v5
	v_add_f32_e32 v2, v18, v17
	v_add_f32_e32 v3, v16, v15
	v_add_f32_e32 v2, v2, v3
	v_add_f32_e32 v3, v14, v13
	v_add_f32_e32 v4, v12, v0
	v_add_f32_e32 v3, v3, v4
	v_add_f32_e32 v2, v2, v3
	v_add_f32_e32 v2, v6, v2
	ds_swizzle_b32 v3, v2 offset:swizzle(SWAP,1)
	v_lshl_add_u64 v[10:11], v[86:87], 0, s[6:7]
	s_mov_b32 s6, 4
	s_waitcnt lgkmcnt(0)
	v_add_f32_e32 v2, v2, v3
	ds_swizzle_b32 v3, v2 offset:swizzle(SWAP,2)
	s_waitcnt lgkmcnt(0)
	v_add_f32_e32 v2, v2, v3
	ds_swizzle_b32 v3, v2 offset:swizzle(SWAP,4)
	s_waitcnt lgkmcnt(0)
	v_add_f32_e32 v2, v2, v3
	ds_swizzle_b32 v3, v2 offset:swizzle(SWAP,8)
	s_waitcnt lgkmcnt(0)
	v_add_f32_e32 v2, v2, v3
	ds_swizzle_b32 v3, v2 offset:swizzle(SWAP,16)
	s_waitcnt lgkmcnt(0)
	v_add_f32_e32 v2, v2, v3
	v_mov_b32_e32 v3, v2
	s_nop 1
	v_permlane32_swap_b32_e32 v2, v3
	v_add_f32_e32 v2, v2, v3
	v_fmac_f32_e32 v45, 0xba000000, v2
	v_fmac_f32_e32 v44, 0xba000000, v2
	v_mul_f32_e32 v3, v45, v45
	v_fmac_f32_e32 v3, v44, v44
	v_fmac_f32_e32 v46, 0xba000000, v2
	v_fmac_f32_e32 v3, v46, v46
	v_fmac_f32_e32 v47, 0xba000000, v2
	v_fmac_f32_e32 v3, v47, v47
	v_fmac_f32_e32 v48, 0xba000000, v2
	v_fmac_f32_e32 v3, v48, v48
	v_fmac_f32_e32 v49, 0xba000000, v2
	v_fmac_f32_e32 v3, v49, v49
	v_fmac_f32_e32 v52, 0xba000000, v2
	v_fmac_f32_e32 v3, v52, v52
	v_fmac_f32_e32 v53, 0xba000000, v2
	v_fmac_f32_e32 v3, v53, v53
	v_fmac_f32_e32 v35, 0xba000000, v2
	v_fmac_f32_e32 v3, v35, v35
	v_fmac_f32_e32 v34, 0xba000000, v2
	v_fmac_f32_e32 v3, v34, v34
	v_fmac_f32_e32 v33, 0xba000000, v2
	v_fmac_f32_e32 v3, v33, v33
	v_fmac_f32_e32 v32, 0xba000000, v2
	v_fmac_f32_e32 v3, v32, v32
	v_fmac_f32_e32 v31, 0xba000000, v2
	v_fmac_f32_e32 v3, v31, v31
	v_fmac_f32_e32 v30, 0xba000000, v2
	v_fmac_f32_e32 v3, v30, v30
	v_fmac_f32_e32 v29, 0xba000000, v2
	v_fmac_f32_e32 v3, v29, v29
	v_fmac_f32_e32 v28, 0xba000000, v2
	v_fmac_f32_e32 v3, v28, v28
	v_fmac_f32_e32 v27, 0xba000000, v2
	v_fmac_f32_e32 v3, v27, v27
	v_fmac_f32_e32 v26, 0xba000000, v2
	v_fmac_f32_e32 v3, v26, v26
	v_fmac_f32_e32 v25, 0xba000000, v2
	v_fmac_f32_e32 v3, v25, v25
	v_fmac_f32_e32 v24, 0xba000000, v2
	v_fmac_f32_e32 v3, v24, v24
	v_fmac_f32_e32 v23, 0xba000000, v2
	v_fmac_f32_e32 v3, v23, v23
	v_fmac_f32_e32 v22, 0xba000000, v2
	v_fmac_f32_e32 v3, v22, v22
	v_fmac_f32_e32 v21, 0xba000000, v2
	v_fmac_f32_e32 v3, v21, v21
	v_fmac_f32_e32 v20, 0xba000000, v2
	v_fmac_f32_e32 v3, v20, v20
	v_fmac_f32_e32 v18, 0xba000000, v2
	v_fmac_f32_e32 v3, v18, v18
	v_fmac_f32_e32 v17, 0xba000000, v2
	v_fmac_f32_e32 v3, v17, v17
	v_fmac_f32_e32 v16, 0xba000000, v2
	v_fmac_f32_e32 v3, v16, v16
	v_fmac_f32_e32 v15, 0xba000000, v2
	v_fmac_f32_e32 v3, v15, v15
	v_fmac_f32_e32 v14, 0xba000000, v2
	v_fmac_f32_e32 v3, v14, v14
	v_fmac_f32_e32 v13, 0xba000000, v2
	v_fmac_f32_e32 v3, v13, v13
	v_fmac_f32_e32 v12, 0xba000000, v2
	v_fmac_f32_e32 v3, v12, v12
	v_fmac_f32_e32 v0, 0xba000000, v2
	v_fmac_f32_e32 v3, v0, v0
	s_nop 1
	s_waitcnt lgkmcnt(0)
	v_add_f32_dpp v2, v3, v3 quad_perm:[1,0,3,2] row_mask:0xf bank_mask:0xf
	s_nop 1
	s_waitcnt lgkmcnt(0)
	v_add_f32_dpp v2, v2, v2 quad_perm:[2,3,0,1] row_mask:0xf bank_mask:0xf
	s_nop 1
	s_waitcnt lgkmcnt(0)
	v_add_f32_dpp v2, v2, v2 row_half_mirror row_mask:0xf bank_mask:0xf
	s_nop 1
	s_waitcnt lgkmcnt(0)
	v_add_f32_dpp v2, v2, v2 row_mirror row_mask:0xf bank_mask:0xf
	ds_swizzle_b32 v3, v2 offset:swizzle(SWAP,16)
	s_waitcnt lgkmcnt(0)
	v_add_f32_e32 v2, v2, v3
	v_mov_b32_e32 v3, v2
	s_nop 1
	v_permlane32_swap_b32_e32 v2, v3
	v_add_f32_e32 v2, v2, v3
	v_fmamk_f32 v2, v2, 0x3a000000, v210
	v_cmp_gt_f32_e32 vcc, s25, v2
	v_mul_f32_e32 v3, 0x4f800000, v2
	s_nop 0
	v_cndmask_b32_e32 v2, v2, v3, vcc
	v_sqrt_f32_e32 v3, v2
	s_nop 0
	v_add_u32_e32 v4, -1, v3
	v_fma_f32 v5, -v4, v3, v2
	v_cmp_ge_f32_e64 s[58:59], 0, v5
	v_add_u32_e32 v5, 1, v3
	s_nop 0
	v_cndmask_b32_e64 v4, v3, v4, s[58:59]
	v_fma_f32 v3, -v5, v3, v2
	v_cmp_lt_f32_e64 s[58:59], 0, v3
	s_nop 1
	v_cndmask_b32_e64 v3, v4, v5, s[58:59]
	v_mul_f32_e32 v4, 0x37800000, v3
	v_cndmask_b32_e32 v3, v3, v4, vcc
	v_cmp_class_f32_e32 vcc, v2, v211
	s_nop 1
	v_cndmask_b32_e32 v2, v3, v2, vcc
	v_div_scale_f32 v3, s[20:21], v2, v2, 1.0
	v_rcp_f32_e32 v4, v3
	s_nop 0
	v_fma_f32 v5, -v3, v4, 1.0
	v_fmac_f32_e32 v4, v5, v4
	v_div_scale_f32 v5, vcc, 1.0, v2, 1.0
	v_mul_f32_e32 v6, v5, v4
	v_fma_f32 v7, -v3, v6, v5
	v_fmac_f32_e32 v6, v7, v4
	v_fma_f32 v3, -v3, v6, v5
	v_div_fmas_f32 v3, v3, v4, v6
	v_div_fixup_f32 v19, v3, v2, 1.0
	v_mul_f32_e32 v44, v44, v19
	v_mul_f32_e32 v31, v31, v19
	v_mul_f32_e32 v35, v35, v19
	v_mul_f32_e32 v34, v34, v19
	v_mul_f32_e32 v33, v33, v19
	v_mul_f32_e32 v32, v32, v19
	v_mul_f32_e32 v23, v23, v19
	v_mul_f32_e32 v27, v27, v19
	v_mul_f32_e32 v26, v26, v19
	v_mul_f32_e32 v25, v25, v19
	v_mul_f32_e32 v24, v24, v19
	v_mul_f32_e32 v15, v15, v19
	v_mul_f32_e32 v18, v18, v19
	v_mul_f32_e32 v17, v17, v19
	v_mul_f32_e32 v16, v16, v19
	v_mul_f32_e32 v0, v0, v19
	s_and_b64 vcc, exec, s[4:5]
	s_mov_b64 s[4:5], 0
	s_waitcnt vmcnt(63)
	v_fma_f32 v40, v182, v44, v190
	v_mul_f32_e32 v6, v45, v19
	v_fma_f32 v41, v183, v6, v191
	v_mul_f32_e32 v7, v47, v19
	v_fma_f32 v9, v185, v7, v193
	v_mul_f32_e32 v7, v48, v19
	v_fma_f32 v7, v186, v7, v194
	v_mul_f32_e32 v2, v49, v19
	v_fma_f32 v3, v187, v2, v195
	v_mul_f32_e32 v2, v52, v19
	v_mul_f32_e32 v6, v46, v19
	v_fma_f32 v4, v188, v2, v196
	v_mul_f32_e32 v2, v53, v19
	v_cvt_pk_bf16_f32 v36, v40, v41
	v_fma_f32 v6, v184, v6, v192
	v_fma_f32 v5, v189, v2, v197
	v_cvt_pk_bf16_f32 v37, v6, v9
	v_cvt_pk_bf16_f32 v38, v7, v3
	v_cvt_pk_bf16_f32 v39, v4, v5
	global_store_dwordx4 v[50:51], v[36:39], off
	v_med3_f32 v8, v40, s19, v229
	v_mov_b32_e32 v2, v1
	v_med3_f32 v36, v41, s19, v229
	v_cvt_pk_fp8_f32 v2, v8, v36
	v_med3_f32 v6, v6, s19, v229
	v_med3_f32 v8, v9, s19, v229
	v_med3_f32 v4, v4, s19, v229
	v_cvt_pk_fp8_f32 v2, v6, v8 op_sel:[0,0,1]
	v_med3_f32 v6, v7, s19, v229
	v_med3_f32 v7, v3, s19, v229
	v_mov_b32_e32 v3, v1
	v_cvt_pk_fp8_f32 v3, v6, v7
	v_med3_f32 v5, v5, s19, v229
	v_cvt_pk_fp8_f32 v3, v4, v5 op_sel:[0,0,1]
	global_store_dwordx2 v[10:11], v[2:3], off
	s_nop 0
	s_waitcnt vmcnt(63)
	v_fma_f32 v31, v31, v202, v212
	v_mul_f32_e32 v2, v30, v19
	v_fma_f32 v3, v2, v203, v213
	v_mul_f32_e32 v2, v29, v19
	s_waitcnt vmcnt(63)
	v_fma_f32 v35, v35, v198, v206
	v_fma_f32 v34, v34, v199, v207
	v_fma_f32 v33, v33, v200, v208
	v_fma_f32 v43, v32, v201, v209
	v_fma_f32 v4, v2, v204, v214
	v_mul_f32_e32 v2, v28, v19
	v_cvt_pk_bf16_f32 v6, v35, v34
	v_cvt_pk_bf16_f32 v7, v33, v43
	v_fma_f32 v5, v2, v205, v215
	v_cvt_pk_bf16_f32 v8, v31, v3
	v_cvt_pk_bf16_f32 v9, v4, v5
	global_store_dwordx4 v[50:51], v[6:9], off offset:1024
	v_mov_b32_e32 v2, v1
	v_med3_f32 v4, v4, s19, v229
	v_med3_f32 v6, v35, s19, v229
	v_med3_f32 v7, v34, s19, v229
	v_cvt_pk_fp8_f32 v2, v6, v7
	v_med3_f32 v6, v33, s19, v229
	v_med3_f32 v7, v43, s19, v229
	v_med3_f32 v5, v5, s19, v229
	v_cvt_pk_fp8_f32 v2, v6, v7 op_sel:[0,0,1]
	v_med3_f32 v6, v31, s19, v229
	v_med3_f32 v7, v3, s19, v229
	v_mov_b32_e32 v3, v1
	v_cvt_pk_fp8_f32 v3, v6, v7
	v_cvt_pk_fp8_f32 v3, v4, v5 op_sel:[0,0,1]
	global_store_dwordx2 v[10:11], v[2:3], off offset:512
	s_nop 0
	s_waitcnt vmcnt(63)
	v_fma_f32 v23, v23, v220, v240
	v_mul_f32_e32 v2, v22, v19
	v_fma_f32 v3, v2, v221, v241
	v_mul_f32_e32 v2, v21, v19
	s_waitcnt vmcnt(63)
	v_fma_f32 v27, v27, v216, v224
	v_fma_f32 v26, v26, v217, v225
	v_fma_f32 v25, v25, v218, v226
	v_fma_f32 v35, v24, v219, v227
	v_fma_f32 v4, v2, v222, v242
	v_mul_f32_e32 v2, v20, v19
	v_cvt_pk_bf16_f32 v6, v27, v26
	v_cvt_pk_bf16_f32 v7, v25, v35
	v_fma_f32 v5, v2, v223, v243
	v_cvt_pk_bf16_f32 v8, v23, v3
	v_cvt_pk_bf16_f32 v9, v4, v5
	global_store_dwordx4 v[50:51], v[6:9], off offset:2048
	v_mov_b32_e32 v2, v1
	v_med3_f32 v4, v4, s19, v229
	v_med3_f32 v6, v27, s19, v229
	v_med3_f32 v7, v26, s19, v229
	v_cvt_pk_fp8_f32 v2, v6, v7
	v_med3_f32 v6, v25, s19, v229
	v_med3_f32 v7, v35, s19, v229
	v_med3_f32 v5, v5, s19, v229
	v_cvt_pk_fp8_f32 v2, v6, v7 op_sel:[0,0,1]
	v_med3_f32 v6, v23, s19, v229
	v_med3_f32 v7, v3, s19, v229
	v_mov_b32_e32 v3, v1
	v_cvt_pk_fp8_f32 v3, v6, v7
	v_cvt_pk_fp8_f32 v3, v4, v5 op_sel:[0,0,1]
	global_store_dwordx2 v[10:11], v[2:3], off offset:1024
	s_nop 0
	s_waitcnt vmcnt(63)
	v_fma_f32 v23, v0, v235, v251
	s_waitcnt vmcnt(63)
	v_fma_f32 v27, v15, v247, v239
	v_mul_f32_e32 v9, v14, v19
	v_fma_f32 v9, v9, v232, v248
	v_mul_f32_e32 v2, v13, v19
	v_fma_f32 v13, v2, v233, v249
	v_mul_f32_e32 v2, v12, v19
	v_fma_f32 v6, v18, v244, v236
	v_fma_f32 v7, v17, v245, v237
	v_fma_f32 v8, v16, v246, v238
	v_fma_f32 v12, v2, v234, v250
	v_cvt_pk_bf16_f32 v2, v6, v7
	v_cvt_pk_bf16_f32 v3, v8, v27
	v_cvt_pk_bf16_f32 v4, v9, v13
	v_cvt_pk_bf16_f32 v5, v12, v23
	global_store_dwordx4 v[50:51], v[2:5], off offset:3072
	v_med3_f32 v0, v6, s19, v229
	s_nop 0
	v_med3_f32 v3, v7, s19, v229
	v_mov_b32_e32 v2, v1
	v_cvt_pk_fp8_f32 v2, v0, v3
	v_med3_f32 v0, v8, s19, v229
	v_med3_f32 v3, v27, s19, v229
	v_med3_f32 v4, v13, s19, v229
	v_cvt_pk_fp8_f32 v2, v0, v3 op_sel:[0,0,1]
	v_med3_f32 v0, v9, s19, v229
	v_mov_b32_e32 v3, v1
	v_cvt_pk_fp8_f32 v3, v0, v4
	v_med3_f32 v0, v12, s19, v229
	v_med3_f32 v4, v23, s19, v229
	v_cvt_pk_fp8_f32 v3, v0, v4 op_sel:[0,0,1]
	global_store_dwordx2 v[10:11], v[2:3], off offset:1536
	s_cbranch_vccnz .LBB0_881
	v_mov_b32_e32 v234, 0xff800000
	v_mov_b32_e32 v235, 64
	v_mov_b64_e32 v[236:237], 0x200
	v_mov_b32_e32 v239, 0x3d800000
	v_mov_b64_e32 v[248:249], 0x1ff
	s_barrier
	s_and_saveexec_b64 s[4:5], s[56:57]
	ds_write_b32 v117, v1
	s_or_b64 exec, exec, s[4:5]
	v_ashrrev_i32_e32 v91, 31, v90
	v_lshlrev_b64 v[2:3], 12, v[90:91]
	v_lshl_add_u64 v[94:95], v[88:89], 0, v[2:3]
	v_mov_b32_e32 v2, 0
	s_mov_b64 s[4:5], 0
	v_mov_b32_e32 v3, v2
	v_mov_b32_e32 v4, v2
	v_mov_b32_e32 v5, v2
	v_mov_b32_e32 v6, v2
	v_mov_b32_e32 v7, v2
	v_mov_b32_e32 v8, v2
	v_mov_b32_e32 v9, v2
	v_mov_b32_e32 v10, v2
	v_mov_b32_e32 v11, v2
	v_mov_b32_e32 v12, v2
	v_mov_b32_e32 v13, v2
	v_mov_b32_e32 v14, v2
	v_mov_b32_e32 v15, v2
	v_mov_b32_e32 v16, v2
	v_mov_b32_e32 v17, v2
	v_mov_b32_e32 v18, v2
	v_mov_b32_e32 v19, v2
	v_mov_b32_e32 v20, v2
	v_mov_b32_e32 v21, v2
	v_mov_b32_e32 v22, v2
	v_mov_b32_e32 v23, v2
	v_mov_b32_e32 v24, v2
	v_mov_b32_e32 v25, v2
	v_mov_b32_e32 v38, v2
	v_mov_b32_e32 v39, v2
	v_mov_b32_e32 v40, v2
	v_mov_b32_e32 v41, v2
	v_mov_b32_e32 v50, v2
	v_mov_b32_e32 v51, v2
	v_mov_b32_e32 v52, v2
	v_mov_b32_e32 v53, v2
	v_mov_b32_e32 v26, v2
	v_mov_b32_e32 v27, v2
	v_mov_b32_e32 v28, v2
	v_mov_b32_e32 v29, v2
	v_mov_b32_e32 v30, v2
	v_mov_b32_e32 v31, v2
	v_mov_b32_e32 v32, v2
	v_mov_b32_e32 v33, v2
	v_mov_b32_e32 v34, v2
	v_mov_b32_e32 v35, v2
	v_mov_b32_e32 v36, v2
	v_mov_b32_e32 v37, v2
	v_mov_b32_e32 v42, v2
	v_mov_b32_e32 v43, v2
	v_mov_b32_e32 v44, v2
	v_mov_b32_e32 v45, v2
	v_mov_b32_e32 v46, v2
	v_mov_b32_e32 v47, v2
	v_mov_b32_e32 v48, v2
	v_mov_b32_e32 v49, v2
	v_mov_b32_e32 v54, v2
	v_mov_b32_e32 v55, v2
	v_mov_b32_e32 v56, v2
	v_mov_b32_e32 v57, v2
	v_mov_b32_e32 v58, v2
	v_mov_b32_e32 v59, v2
	v_mov_b32_e32 v60, v2
	v_mov_b32_e32 v61, v2
	v_mov_b32_e32 v62, v2
	v_mov_b32_e32 v63, v2
	v_mov_b32_e32 v64, v2
	v_mov_b32_e32 v65, v2

.LBB0_888:
	s_or_b32 s4, s12, s71
	v_lshl_add_u32 v2, s4, 8, v113
	ds_read_b32 v2, v2
	s_mov_b32 s5, 0x42ce8ed0
	s_waitcnt lgkmcnt(0)
	v_mul_f32_e32 v3, 0xbfb8aa3b, v2
	v_fma_f32 v4, v2, s24, -v3
	v_rndne_f32_e32 v5, v3
	v_fmac_f32_e32 v4, 0xb2a5705f, v2
	v_sub_f32_e32 v3, v3, v5
	v_add_f32_e32 v3, v3, v4
	v_exp_f32_e32 v3, v3
	v_cvt_i32_f32_e32 v4, v5
	v_cmp_nlt_f32_e32 vcc, s5, v2
	s_mov_b32 s5, 0xc2b17218
	v_ldexp_f32 v3, v3, v4
	v_cndmask_b32_e32 v3, 0, v3, vcc
	v_cmp_ngt_f32_e32 vcc, s5, v2
	s_nop 1
	v_cndmask_b32_e32 v2, v231, v3, vcc
	v_add_f32_e32 v2, 1.0, v2
	v_div_scale_f32 v3, s[6:7], v2, v2, 1.0
	v_rcp_f32_e32 v4, v3
	s_nop 0
	v_fma_f32 v5, -v3, v4, 1.0
	v_fmac_f32_e32 v4, v5, v4
	v_div_scale_f32 v5, vcc, 1.0, v2, 1.0
	v_mul_f32_e32 v6, v5, v4
	v_fma_f32 v7, -v3, v6, v5
	v_fmac_f32_e32 v6, v7, v4
	v_fma_f32 v3, -v3, v6, v5
	v_div_fmas_f32 v3, v3, v4, v6
	v_div_fixup_f32 v2, v3, v2, 1.0
	v_add_f32_e32 v3, v112, v2
	s_nop 1
	s_waitcnt lgkmcnt(0)
	v_max_f32_e32 v4, v3, v3
	s_nop 1
	v_max_f32_dpp v4, v4, v4 quad_perm:[1,0,3,2] row_mask:0xf bank_mask:0xf
	s_nop 1
	s_waitcnt lgkmcnt(0)
	v_max_f32_e32 v5, v4, v4
	s_nop 1
	v_max_f32_dpp v4, v5, v5 quad_perm:[2,3,0,1] row_mask:0xf bank_mask:0xf
	s_nop 1
	s_waitcnt lgkmcnt(0)
	v_max_f32_e32 v5, v4, v4
	s_nop 1
	v_max_f32_dpp v6, v5, v5 row_half_mirror row_mask:0xf bank_mask:0xf
	v_cmp_eq_f32_e32 vcc, v3, v6
	s_nop 1
	v_lshrrev_b64 v[4:5], v68, vcc
	v_ffbl_b32_sdwa v4, v4 dst_sel:DWORD dst_unused:UNUSED_PAD src0_sel:BYTE_0
	v_cmp_ne_u32_e32 vcc, v114, v4
	s_nop 1
	v_cndmask_b32_e32 v4, v234, v3, vcc
	s_nop 1
	s_waitcnt lgkmcnt(0)
	v_max_f32_e32 v5, v4, v4
	s_nop 1
	v_max_f32_dpp v4, v5, v5 quad_perm:[1,0,3,2] row_mask:0xf bank_mask:0xf
	s_nop 1
	s_waitcnt lgkmcnt(0)
	v_max_f32_e32 v5, v4, v4
	s_nop 1
	v_max_f32_dpp v4, v5, v5 quad_perm:[2,3,0,1] row_mask:0xf bank_mask:0xf
	s_nop 1
	s_waitcnt lgkmcnt(0)
	v_max_f32_e32 v5, v4, v4
	s_nop 1
	v_max_f32_dpp v4, v5, v5 row_half_mirror row_mask:0xf bank_mask:0xf
	v_add_f32_e32 v4, v6, v4
	s_nop 0
	v_readlane_b32 s5, v4, 0
	s_nop 1
	v_cmp_eq_f32_e64 s[58:59], s5, v4
	v_cmp_gt_f32_e32 vcc, s5, v4
	s_and_b64 s[6:7], s[40:41], s[58:59]
	v_readlane_b32 s5, v4, 8
	s_or_b64 s[6:7], vcc, s[6:7]
	v_cndmask_b32_e64 v5, 0, 1, s[6:7]
	v_cmp_eq_f32_e64 s[58:59], s5, v4
	v_cmp_gt_f32_e32 vcc, s5, v4
	s_and_b64 s[6:7], s[42:43], s[58:59]
	v_readlane_b32 s5, v4, 16
	s_or_b64 s[6:7], vcc, s[6:7]
	v_cndmask_b32_e64 v6, 0, 1, s[6:7]
	v_cmp_eq_f32_e64 s[58:59], s5, v4
	v_cmp_gt_f32_e32 vcc, s5, v4
	s_and_b64 s[6:7], s[44:45], s[58:59]
	v_readlane_b32 s5, v4, 24
	s_or_b64 s[6:7], vcc, s[6:7]
	v_add_u32_e32 v5, v5, v6
	v_cmp_eq_f32_e64 s[58:59], s5, v4
	v_cndmask_b32_e64 v6, 0, 1, s[6:7]
	v_cmp_gt_f32_e32 vcc, s5, v4
	s_and_b64 s[6:7], s[46:47], s[58:59]
	v_readlane_b32 s5, v4, 32
	s_or_b64 s[6:7], vcc, s[6:7]
	v_cndmask_b32_e64 v7, 0, 1, s[6:7]
	v_cmp_eq_f32_e64 s[58:59], s5, v4
	v_cmp_gt_f32_e32 vcc, s5, v4
	s_and_b64 s[6:7], s[48:49], s[58:59]
	v_readlane_b32 s5, v4, 40
	s_or_b64 s[6:7], vcc, s[6:7]
	v_add3_u32 v5, v5, v6, v7
	v_cmp_eq_f32_e64 s[58:59], s5, v4
	v_cndmask_b32_e64 v6, 0, 1, s[6:7]
	v_cmp_gt_f32_e32 vcc, s5, v4
	s_and_b64 s[6:7], s[50:51], s[58:59]
	v_readlane_b32 s5, v4, 48
	s_or_b64 s[6:7], vcc, s[6:7]
	v_cndmask_b32_e64 v7, 0, 1, s[6:7]
	v_cmp_eq_f32_e64 s[58:59], s5, v4
	v_cmp_gt_f32_e32 vcc, s5, v4
	s_and_b64 s[6:7], s[52:53], s[58:59]
	v_readlane_b32 s5, v4, 56
	s_or_b64 s[6:7], vcc, s[6:7]
	v_add3_u32 v5, v5, v6, v7
	v_cmp_eq_f32_e64 s[58:59], s5, v4
	v_cndmask_b32_e64 v6, 0, 1, s[6:7]
	v_cmp_gt_f32_e32 vcc, s5, v4
	s_and_b64 s[6:7], s[54:55], s[58:59]
	s_or_b64 s[6:7], vcc, s[6:7]
	v_cndmask_b32_e64 v4, 0, 1, s[6:7]
	v_add3_u32 v4, v5, v6, v4
	v_cmp_gt_u32_e32 vcc, 4, v4
	s_mov_b32 s5, 0
	v_mov_b32_e32 v4, 0
	v_cndmask_b32_e32 v3, v234, v3, vcc
.LBB0_889:
	s_nop 0
	v_readlane_b32 s6, v3, s5
	v_cmp_lt_i32_e64 s[60:61], s5, v66
	s_nop 0
	v_cmp_eq_f32_e64 s[58:59], s6, v3
	v_cmp_gt_f32_e32 vcc, s6, v3
	s_and_b64 s[6:7], s[60:61], s[58:59]
	s_or_b64 s[6:7], vcc, s[6:7]
	v_cndmask_b32_e64 v5, 0, 1, s[6:7]
	s_add_i32 s6, s5, 1
	v_readlane_b32 s7, v3, s6
	v_cmp_lt_i32_e64 s[60:61], s6, v66
	s_nop 0
	v_cmp_eq_f32_e64 s[58:59], s7, v3
	v_cmp_gt_f32_e32 vcc, s7, v3
	s_and_b64 s[6:7], s[60:61], s[58:59]
	s_or_b64 vcc, vcc, s[6:7]
	s_add_i32 s6, s5, 2
	v_readlane_b32 s7, v3, s6
	v_addc_co_u32_e32 v4, vcc, v4, v5, vcc
	s_nop 0
	v_cmp_eq_f32_e64 s[58:59], s7, v3
	v_cmp_lt_i32_e64 s[60:61], s6, v66
	v_cmp_gt_f32_e32 vcc, s7, v3
	s_and_b64 s[6:7], s[60:61], s[58:59]
	s_or_b64 s[6:7], vcc, s[6:7]
	v_cndmask_b32_e64 v5, 0, 1, s[6:7]
	s_add_i32 s6, s5, 3
	v_readlane_b32 s7, v3, s6
	v_cmp_lt_i32_e64 s[60:61], s6, v66
	s_add_i32 s5, s5, 4
	v_cmp_eq_f32_e64 s[58:59], s7, v3
	v_cmp_gt_f32_e32 vcc, s7, v3
	s_and_b64 s[6:7], s[60:61], s[58:59]
	s_or_b64 vcc, vcc, s[6:7]
	v_addc_co_u32_e32 v4, vcc, v4, v5, vcc
	s_cmp_eq_u32 s5, 64
	s_cbranch_scc0 .LBB0_889
	s_add_i32 s6, s4, s30
	v_cmp_gt_u32_e64 s[4:5], 8, v4
	s_nop 1
	v_cndmask_b32_e64 v3, 0, v2, s[4:5]
	s_nop 1
	s_waitcnt lgkmcnt(0)
	v_add_f32_dpp v3, v3, v3 quad_perm:[1,0,3,2] row_mask:0xf bank_mask:0xf
	s_nop 1
	s_waitcnt lgkmcnt(0)
	v_add_f32_dpp v3, v3, v3 quad_perm:[2,3,0,1] row_mask:0xf bank_mask:0xf
	s_nop 1
	s_waitcnt lgkmcnt(0)
	v_add_f32_dpp v3, v3, v3 row_half_mirror row_mask:0xf bank_mask:0xf
	s_nop 1
	s_waitcnt lgkmcnt(0)
	v_add_f32_dpp v3, v3, v3 row_mirror row_mask:0xf bank_mask:0xf
	ds_swizzle_b32 v4, v3 offset:swizzle(SWAP,16)
	s_waitcnt lgkmcnt(0)
	v_add_f32_e32 v3, v3, v4
	v_mov_b32_e32 v4, v3
	s_nop 1
	v_permlane32_swap_b32_e32 v3, v4
	s_and_saveexec_b64 s[58:59], s[4:5]
	s_cbranch_execz .LBB0_892
	v_add_f32_e32 v3, v3, v4
	v_div_scale_f32 v4, s[20:21], v3, v3, v2
	v_rcp_f32_e32 v5, v4
	v_div_scale_f32 v6, vcc, v2, v3, v2
	s_ashr_i32 s7, s6, 31
	v_fma_f32 v7, -v4, v5, 1.0
	v_fmac_f32_e32 v5, v7, v5
	v_mul_f32_e32 v7, v6, v5
	v_fma_f32 v8, -v4, v7, v6
	v_fmac_f32_e32 v7, v8, v5
	v_fma_f32 v4, -v4, v7, v6
	v_div_fmas_f32 v4, v4, v5, v7
	v_div_fixup_f32 v2, v4, v3, v2
	v_and_b32_e32 v4, s4, v70
	v_and_b32_e32 v3, s5, v69
	v_bcnt_u32_b32 v4, v4, 0
	s_lshl_b64 s[20:21], s[6:7], 5
	v_bcnt_u32_b32 v3, v3, v4
	s_add_u32 s20, s68, s20
	v_mul_f32_e32 v2, 0x40200000, v2
	s_addc_u32 s21, s69, s21
	v_lshlrev_b32_e32 v3, 2, v3
	global_store_dword v3, v2, s[20:21]

.LBB0_1355:
	v_mov_b32_e32 v23, v61
	v_lshlrev_b32_e32 v0, 4, v23
	v_lshl_add_u64 v[10:11], s[52:53], 0, v[0:1]
	v_lshl_add_u64 v[2:3], s[10:11], 0, v[10:11]
	v_add_co_u32_e32 v12, vcc, s26, v2
	s_nop 1
	v_addc_co_u32_e32 v13, vcc, 0, v3, vcc
	global_load_dwordx4 v[240:243], v[12:13], off
	s_add_i32 s38, s44, 0x24000
	s_ashr_i32 s39, s38, 31
	s_lshl_b64 s[38:39], s[38:39], 11
	s_waitcnt vmcnt(9)
	v_lshlrev_b32_e32 v36, 3, v23
	s_add_u32 s38, s46, s38
	s_addc_u32 s39, s47, s39
	v_mov_b32_e32 v0, v36
	v_lshl_add_u64 v[18:19], s[46:47], 0, v[0:1]
	global_load_dwordx2 v[16:17], v36, s[38:39]
	s_mov_b32 s30, 0x3d800000
	s_mov_b64 s[58:59], -1
	v_readfirstlane_b32 s56, v194
	s_ashr_i32 s57, s56, 31
	s_lshl_b64 s[56:57], s[56:57], 11
	v_lshl_add_u64 v[20:21], v[18:19], 0, s[56:57]
	global_load_dwordx2 v[14:15], v[20:21], off
	global_load_dwordx4 v[6:9], v[12:13], off offset:1024
	global_load_dwordx2 v[30:31], v36, s[38:39] offset:512
	global_load_dwordx2 v[64:65], v36, s[38:39] offset:1024
	global_load_dwordx2 v[54:55], v36, s[38:39] offset:1536
	v_readfirstlane_b32 s38, v195
	s_ashr_i32 s39, s38, 31
	s_lshl_b64 s[38:39], s[38:39], 11
	v_lshl_add_u64 v[40:41], v[18:19], 0, s[38:39]
	global_load_dwordx2 v[42:43], v[40:41], off
	v_readfirstlane_b32 s27, v202
	v_readfirstlane_b32 s38, v196
	s_ashr_i32 s39, s38, 31
	s_lshl_b64 s[38:39], s[38:39], 11
	v_lshl_add_u64 v[46:47], v[18:19], 0, s[38:39]
	v_readfirstlane_b32 s38, v197
	s_ashr_i32 s39, s38, 31
	s_lshl_b64 s[38:39], s[38:39], 11
	v_lshl_add_u64 v[50:51], v[18:19], 0, s[38:39]
	global_load_dwordx2 v[48:49], v[46:47], off
	global_load_dwordx2 v[58:59], v[50:51], off
	global_load_dwordx2 v[102:103], v[20:21], off offset:512
	global_load_dwordx2 v[160:161], v[20:21], off offset:1024
	v_mul_f32_e32 v60, s27, v239
	v_readfirstlane_b32 s38, v198
	s_ashr_i32 s39, s38, 31
	s_lshl_b64 s[38:39], s[38:39], 11
	v_lshl_add_u64 v[62:63], v[18:19], 0, s[38:39]
	global_load_dwordx2 v[68:69], v[62:63], off
	global_load_dwordx2 v[96:97], v[20:21], off offset:1536
	v_readfirstlane_b32 s27, v203
	v_readfirstlane_b32 s38, v199
	s_ashr_i32 s39, s38, 31
	s_lshl_b64 s[38:39], s[38:39], 11
	v_lshl_add_u64 v[72:73], v[18:19], 0, s[38:39]
	global_load_dwordx2 v[74:75], v[72:73], off
	v_mul_f32_e32 v2, s27, v239
	v_readfirstlane_b32 s27, v204
	v_readfirstlane_b32 s38, v200
	s_ashr_i32 s39, s38, 31
	s_lshl_b64 s[38:39], s[38:39], 11
	v_lshl_add_u64 v[80:81], v[18:19], 0, s[38:39]
	global_load_dwordx2 v[90:91], v[80:81], off
	v_readfirstlane_b32 s38, v201
	s_ashr_i32 s39, s38, 31
	s_lshl_b64 s[38:39], s[38:39], 11
	v_lshl_add_u64 v[94:95], v[18:19], 0, s[38:39]
	global_load_dwordx2 v[110:111], v[94:95], off
	global_load_dwordx2 v[114:115], v[40:41], off offset:512
	global_load_dwordx2 v[120:121], v[46:47], off offset:512
	global_load_dwordx2 v[182:183], v[40:41], off offset:1024
	global_load_dwordx2 v[98:99], v[40:41], off offset:1536
	global_load_dwordx2 v[126:127], v[50:51], off offset:512
	global_load_dwordx2 v[134:135], v[62:63], off offset:512
	global_load_dwordx2 v[184:185], v[46:47], off offset:1024
	global_load_dwordx2 v[100:101], v[46:47], off offset:1536
	global_load_dwordx2 v[144:145], v[72:73], off offset:512
	global_load_dwordx2 v[158:159], v[80:81], off offset:512
	global_load_dwordx2 v[186:187], v[50:51], off offset:1024
	global_load_dwordx2 v[106:107], v[50:51], off offset:1536
	global_load_dwordx2 v[188:189], v[94:95], off offset:512
	global_load_dwordx2 v[190:191], v[62:63], off offset:1024
	global_load_dwordx2 v[104:105], v[62:63], off offset:1536
	global_load_dwordx2 v[192:193], v[72:73], off offset:1024
	global_load_dwordx2 v[108:109], v[72:73], off offset:1536
	global_load_dwordx4 v[174:177], v[12:13], off offset:2048
	global_load_dwordx2 v[152:153], v[80:81], off offset:1024
	global_load_dwordx2 v[116:117], v[80:81], off offset:1536
	global_load_dwordx2 v[136:137], v[94:95], off offset:1024
	global_load_dwordx2 v[128:129], v[94:95], off offset:1536
	global_load_dwordx4 v[178:181], v[12:13], off offset:3072
	s_waitcnt vmcnt(38)
	v_lshlrev_b32_e32 v36, 16, v240
	v_and_b32_e32 v37, 0xffff0000, v240
	v_lshlrev_b32_e32 v38, 16, v242
	v_cvt_pk_f32_fp8_e32 v[28:29], v16
	v_cvt_pk_f32_fp8_e32 v[32:33], v17
	v_cvt_pk_f32_fp8_sdwa v[34:35], v16 src0_sel:WORD_1
	v_and_b32_e32 v39, 0xffff0000, v242
	v_mul_f32_e32 v4, s27, v239
	v_readfirstlane_b32 s27, v205
	s_waitcnt vmcnt(33)
	v_cvt_pk_f32_fp8_e32 v[218:219], v54
	v_cvt_pk_f32_fp8_e32 v[224:225], v55
	v_mul_f32_e32 v18, s27, v239
	v_readfirstlane_b32 s27, v206
	v_pk_mul_f32 v[218:219], v[218:219], s[30:31] op_sel_hi:[1,0]
	v_pk_mul_f32 v[224:225], v[224:225], s[30:31] op_sel_hi:[1,0]
	v_mul_f32_e32 v20, s27, v239
	v_readfirstlane_b32 s27, v207
	v_cvt_pk_f32_fp8_sdwa v[52:53], v17 src0_sel:WORD_1
	v_pk_mul_f32 v[16:17], v[28:29], s[30:31] op_sel_hi:[1,0]
	v_mul_f32_e32 v22, s27, v239
	v_readfirstlane_b32 s27, v208
	v_pk_mul_f32 v[28:29], v[32:33], s[30:31] op_sel_hi:[1,0]
	v_pk_mul_f32 v[32:33], v[34:35], s[30:31] op_sel_hi:[1,0]
	v_pk_fma_f32 v[16:17], v[36:37], s[16:17], v[16:17] op_sel_hi:[1,0,1]
	v_cvt_pk_f32_fp8_e32 v[34:35], v14
	v_cvt_pk_f32_fp8_e32 v[36:37], v15
	v_mul_f32_e32 v24, s27, v239
	v_readfirstlane_b32 s27, v209
	v_cvt_pk_f32_fp8_sdwa v[56:57], v14 src0_sel:WORD_1
	v_lshlrev_b32_e32 v44, 16, v241
	v_and_b32_e32 v45, 0xffff0000, v241
	v_pk_fma_f32 v[28:29], v[38:39], s[16:17], v[28:29] op_sel_hi:[1,0,1]
	v_cvt_pk_f32_fp8_sdwa v[14:15], v15 src0_sel:WORD_1
	v_pk_fma_f32 v[38:39], v[60:61], v[34:35], v[16:17] op_sel_hi:[0,1,1]
	v_pk_fma_f32 v[16:17], v[60:61], v[36:37], v[28:29] op_sel_hi:[0,1,1]
	v_pk_fma_f32 v[28:29], v[44:45], s[16:17], v[32:33] op_sel_hi:[1,0,1]
	v_pk_mul_f32 v[32:33], v[52:53], s[30:31] op_sel_hi:[1,0]
	v_pk_fma_f32 v[36:37], v[60:61], v[56:57], v[28:29] op_sel_hi:[0,1,1]
	v_lshlrev_b32_e32 v28, 16, v243
	v_and_b32_e32 v29, 0xffff0000, v243
	v_pk_fma_f32 v[28:29], v[28:29], s[16:17], v[32:33] op_sel_hi:[1,0,1]
	s_waitcnt vmcnt(32)
	v_cvt_pk_f32_fp8_e32 v[56:57], v42
	v_pk_fma_f32 v[14:15], v[60:61], v[14:15], v[28:29] op_sel_hi:[0,1,1]
	v_cvt_pk_f32_fp8_sdwa v[44:45], v42 src0_sel:WORD_1
	v_cvt_pk_f32_fp8_e32 v[32:33], v43
	v_cvt_pk_f32_fp8_sdwa v[28:29], v43 src0_sel:WORD_1
	s_waitcnt vmcnt(31)
	v_cvt_pk_f32_fp8_e32 v[70:71], v48
	v_cvt_pk_f32_fp8_sdwa v[52:53], v48 src0_sel:WORD_1
	s_waitcnt vmcnt(26)
	v_cvt_pk_f32_fp8_e32 v[226:227], v96
	v_cvt_pk_f32_fp8_e32 v[40:41], v49
	v_cvt_pk_f32_fp8_sdwa v[34:35], v49 src0_sel:WORD_1
	v_cvt_pk_f32_fp8_e32 v[78:79], v58
	v_cvt_pk_f32_fp8_sdwa v[66:67], v58 src0_sel:WORD_1
	v_cvt_pk_f32_fp8_e32 v[48:49], v59
	v_cvt_pk_f32_fp8_sdwa v[42:43], v59 src0_sel:WORD_1
	v_cvt_pk_f32_fp8_e32 v[84:85], v68
	v_cvt_pk_f32_fp8_sdwa v[76:77], v68 src0_sel:WORD_1
	v_cvt_pk_f32_fp8_e32 v[58:59], v69
	v_cvt_pk_f32_fp8_sdwa v[46:47], v69 src0_sel:WORD_1
	s_waitcnt vmcnt(25)
	v_cvt_pk_f32_fp8_e32 v[88:89], v74
	v_cvt_pk_f32_fp8_sdwa v[82:83], v74 src0_sel:WORD_1
	v_cvt_pk_f32_fp8_e32 v[68:69], v75
	v_cvt_pk_f32_fp8_sdwa v[50:51], v75 src0_sel:WORD_1
	v_cvt_pk_f32_fp8_sdwa v[112:113], v30 src0_sel:WORD_1
	s_waitcnt vmcnt(24)
	v_cvt_pk_f32_fp8_e32 v[92:93], v90
	v_cvt_pk_f32_fp8_sdwa v[86:87], v90 src0_sel:WORD_1
	v_cvt_pk_f32_fp8_e32 v[74:75], v91
	v_cvt_pk_f32_fp8_sdwa v[62:63], v91 src0_sel:WORD_1
	v_cvt_pk_f32_fp8_e32 v[118:119], v31
	s_waitcnt vmcnt(23)
	v_cvt_pk_f32_fp8_e32 v[94:95], v110
	v_cvt_pk_f32_fp8_sdwa v[90:91], v110 src0_sel:WORD_1
	v_cvt_pk_f32_fp8_e32 v[80:81], v111
	v_cvt_pk_f32_fp8_sdwa v[72:73], v111 src0_sel:WORD_1
	v_cvt_pk_f32_fp8_e32 v[110:111], v30
	v_cvt_pk_f32_fp8_sdwa v[122:123], v31 src0_sel:WORD_1
	s_waitcnt vmcnt(11)
	v_cvt_pk_f32_fp8_e32 v[232:233], v106
	v_cvt_pk_f32_fp8_e32 v[30:31], v102
	v_cvt_pk_f32_fp8_sdwa v[124:125], v102 src0_sel:WORD_1
	v_cvt_pk_f32_fp8_e32 v[130:131], v103
	v_cvt_pk_f32_fp8_sdwa v[132:133], v103 src0_sel:WORD_1
	v_lshlrev_b32_e32 v102, 16, v6
	v_and_b32_e32 v103, 0xffff0000, v6
	s_waitcnt vmcnt(0)
	v_lshlrev_b32_e32 v220, 16, v178
	v_and_b32_e32 v221, 0xffff0000, v178
	v_pk_fma_f32 v[218:219], v[220:221], s[16:17], v[218:219] op_sel_hi:[1,0,1]
	v_cvt_pk_f32_fp8_sdwa v[220:221], v54 src0_sel:WORD_1
	v_pk_fma_f32 v[218:219], v[60:61], v[226:227], v[218:219] op_sel_hi:[0,1,1]
	v_cvt_pk_f32_fp8_e32 v[226:227], v97
	v_cvt_pk_f32_fp8_sdwa v[54:55], v55 src0_sel:WORD_1
	v_lshlrev_b32_e32 v222, 16, v180
	v_and_b32_e32 v223, 0xffff0000, v180
	v_pk_fma_f32 v[222:223], v[222:223], s[16:17], v[224:225] op_sel_hi:[1,0,1]
	v_lshlrev_b32_e32 v180, 16, v181
	v_pk_fma_f32 v[222:223], v[60:61], v[226:227], v[222:223] op_sel_hi:[0,1,1]
	v_cvt_pk_f32_fp8_sdwa v[226:227], v96 src0_sel:WORD_1
	v_cvt_pk_f32_fp8_sdwa v[96:97], v97 src0_sel:WORD_1
	v_and_b32_e32 v181, 0xffff0000, v181
	v_pk_mul_f32 v[54:55], v[54:55], s[30:31] op_sel_hi:[1,0]
	v_pk_mul_f32 v[110:111], v[110:111], s[30:31] op_sel_hi:[1,0]
	v_pk_fma_f32 v[54:55], v[180:181], s[16:17], v[54:55] op_sel_hi:[1,0,1]
	v_cvt_pk_f32_fp8_e32 v[180:181], v98
	v_pk_fma_f32 v[54:55], v[60:61], v[96:97], v[54:55] op_sel_hi:[0,1,1]
	v_cvt_pk_f32_fp8_e32 v[96:97], v100
	v_pk_fma_f32 v[102:103], v[102:103], s[16:17], v[110:111] op_sel_hi:[1,0,1]
	v_pk_fma_f32 v[180:181], v[2:3], v[180:181], v[218:219] op_sel_hi:[0,1,1]
	v_cvt_pk_f32_fp8_e32 v[218:219], v104
	v_pk_fma_f32 v[96:97], v[4:5], v[96:97], v[180:181] op_sel_hi:[0,1,1]
	v_cvt_pk_f32_fp8_e32 v[180:181], v108
	v_pk_fma_f32 v[96:97], v[18:19], v[232:233], v[96:97] op_sel_hi:[0,1,1]
	v_cvt_pk_f32_fp8_e32 v[232:233], v116
	v_pk_fma_f32 v[96:97], v[20:21], v[218:219], v[96:97] op_sel_hi:[0,1,1]
	v_cvt_pk_f32_fp8_e32 v[218:219], v128
	v_pk_fma_f32 v[102:103], v[60:61], v[30:31], v[102:103] op_sel_hi:[0,1,1]
	v_lshlrev_b32_e32 v30, 16, v8
	v_and_b32_e32 v31, 0xffff0000, v8
	v_pk_mul_f32 v[110:111], v[118:119], s[30:31] op_sel_hi:[1,0]
	v_pk_fma_f32 v[96:97], v[22:23], v[180:181], v[96:97] op_sel_hi:[0,1,1]
	v_cvt_pk_f32_fp8_sdwa v[180:181], v98 src0_sel:WORD_1
	v_mul_f32_e32 v26, s27, v239
	v_pk_fma_f32 v[30:31], v[30:31], s[16:17], v[110:111] op_sel_hi:[1,0,1]
	v_lshlrev_b32_e32 v6, 16, v7
	v_and_b32_e32 v7, 0xffff0000, v7
	v_pk_mul_f32 v[110:111], v[112:113], s[30:31] op_sel_hi:[1,0]
	v_lshlrev_b32_e32 v178, 16, v179
	v_and_b32_e32 v179, 0xffff0000, v179
	v_pk_mul_f32 v[220:221], v[220:221], s[30:31] op_sel_hi:[1,0]
	v_pk_fma_f32 v[96:97], v[24:25], v[232:233], v[96:97] op_sel_hi:[0,1,1]
	v_cvt_pk_f32_fp8_sdwa v[232:233], v100 src0_sel:WORD_1
	v_pk_fma_f32 v[6:7], v[6:7], s[16:17], v[110:111] op_sel_hi:[1,0,1]
	v_pk_fma_f32 v[178:179], v[178:179], s[16:17], v[220:221] op_sel_hi:[1,0,1]
	v_pk_fma_f32 v[96:97], v[26:27], v[218:219], v[96:97] op_sel_hi:[0,1,1]
	v_cvt_pk_f32_fp8_sdwa v[218:219], v106 src0_sel:WORD_1
	v_pk_fma_f32 v[110:111], v[60:61], v[124:125], v[6:7] op_sel_hi:[0,1,1]
	v_lshlrev_b32_e32 v6, 16, v9
	v_and_b32_e32 v7, 0xffff0000, v9
	v_pk_mul_f32 v[8:9], v[122:123], s[30:31] op_sel_hi:[1,0]
	v_pk_fma_f32 v[178:179], v[60:61], v[226:227], v[178:179] op_sel_hi:[0,1,1]
	v_pk_fma_f32 v[6:7], v[6:7], s[16:17], v[8:9] op_sel_hi:[1,0,1]
	v_pk_fma_f32 v[178:179], v[2:3], v[180:181], v[178:179] op_sel_hi:[0,1,1]
	v_cvt_pk_f32_fp8_sdwa v[180:181], v104 src0_sel:WORD_1
	v_pk_fma_f32 v[30:31], v[60:61], v[130:131], v[30:31] op_sel_hi:[0,1,1]
	v_pk_fma_f32 v[6:7], v[60:61], v[132:133], v[6:7] op_sel_hi:[0,1,1]
	v_cvt_pk_f32_fp8_e32 v[138:139], v114
	v_cvt_pk_f32_fp8_sdwa v[122:123], v114 src0_sel:WORD_1
	v_cvt_pk_f32_fp8_e32 v[112:113], v115
	v_cvt_pk_f32_fp8_sdwa v[8:9], v115 src0_sel:WORD_1
	v_cvt_pk_f32_fp8_e32 v[146:147], v120
	v_cvt_pk_f32_fp8_sdwa v[130:131], v120 src0_sel:WORD_1
	v_cvt_pk_f32_fp8_e32 v[118:119], v121
	v_cvt_pk_f32_fp8_sdwa v[12:13], v121 src0_sel:WORD_1
	v_cvt_pk_f32_fp8_e32 v[154:155], v126
	v_cvt_pk_f32_fp8_sdwa v[140:141], v126 src0_sel:WORD_1
	v_cvt_pk_f32_fp8_e32 v[124:125], v127
	v_cvt_pk_f32_fp8_sdwa v[114:115], v127 src0_sel:WORD_1
	v_cvt_pk_f32_fp8_e32 v[162:163], v134
	v_cvt_pk_f32_fp8_sdwa v[148:149], v134 src0_sel:WORD_1
	v_cvt_pk_f32_fp8_e32 v[132:133], v135
	v_cvt_pk_f32_fp8_sdwa v[120:121], v135 src0_sel:WORD_1
	v_cvt_pk_f32_fp8_e32 v[166:167], v144
	v_cvt_pk_f32_fp8_sdwa v[156:157], v144 src0_sel:WORD_1
	v_cvt_pk_f32_fp8_e32 v[142:143], v145
	v_cvt_pk_f32_fp8_sdwa v[126:127], v145 src0_sel:WORD_1
	v_cvt_pk_f32_fp8_e32 v[170:171], v158
	v_cvt_pk_f32_fp8_sdwa v[164:165], v158 src0_sel:WORD_1
	v_cvt_pk_f32_fp8_e32 v[150:151], v159
	v_cvt_pk_f32_fp8_sdwa v[134:135], v159 src0_sel:WORD_1
	v_cvt_pk_f32_fp8_e32 v[172:173], v188
	v_cvt_pk_f32_fp8_sdwa v[168:169], v188 src0_sel:WORD_1
	v_cvt_pk_f32_fp8_e32 v[158:159], v189
	v_cvt_pk_f32_fp8_sdwa v[144:145], v189 src0_sel:WORD_1
	v_cvt_pk_f32_fp8_e32 v[188:189], v64
	v_pk_fma_f32 v[178:179], v[4:5], v[232:233], v[178:179] op_sel_hi:[0,1,1]
	v_cvt_pk_f32_fp8_sdwa v[232:233], v108 src0_sel:WORD_1
	v_pk_fma_f32 v[178:179], v[18:19], v[218:219], v[178:179] op_sel_hi:[0,1,1]
	v_cvt_pk_f32_fp8_sdwa v[218:219], v116 src0_sel:WORD_1
	v_cvt_pk_f32_fp8_sdwa v[194:195], v64 src0_sel:WORD_1
	v_cvt_pk_f32_fp8_e32 v[196:197], v65
	v_cvt_pk_f32_fp8_sdwa v[64:65], v65 src0_sel:WORD_1
	v_cvt_pk_f32_fp8_e32 v[198:199], v160
	v_pk_fma_f32 v[178:179], v[20:21], v[180:181], v[178:179] op_sel_hi:[0,1,1]
	v_cvt_pk_f32_fp8_sdwa v[180:181], v128 src0_sel:WORD_1
	v_cvt_pk_f32_fp8_sdwa v[200:201], v160 src0_sel:WORD_1
	v_cvt_pk_f32_fp8_e32 v[202:203], v161
	v_cvt_pk_f32_fp8_sdwa v[160:161], v161 src0_sel:WORD_1
	v_lshlrev_b32_e32 v204, 16, v174
	v_and_b32_e32 v205, 0xffff0000, v174
	v_pk_mul_f32 v[188:189], v[188:189], s[30:31] op_sel_hi:[1,0]
	v_pk_fma_f32 v[178:179], v[22:23], v[232:233], v[178:179] op_sel_hi:[0,1,1]
	v_cvt_pk_f32_fp8_e32 v[232:233], v99
	v_pk_fma_f32 v[188:189], v[204:205], s[16:17], v[188:189] op_sel_hi:[1,0,1]
	v_pk_fma_f32 v[178:179], v[24:25], v[218:219], v[178:179] op_sel_hi:[0,1,1]
	v_cvt_pk_f32_fp8_e32 v[218:219], v101
	v_cvt_pk_f32_fp8_sdwa v[98:99], v99 src0_sel:WORD_1
	v_pk_fma_f32 v[188:189], v[60:61], v[198:199], v[188:189] op_sel_hi:[0,1,1]
	v_lshlrev_b32_e32 v198, 16, v176
	v_and_b32_e32 v199, 0xffff0000, v176
	v_lshlrev_b32_e32 v176, 16, v177
	v_and_b32_e32 v177, 0xffff0000, v177
	v_pk_mul_f32 v[64:65], v[64:65], s[30:31] op_sel_hi:[1,0]
	v_cvt_pk_f32_fp8_sdwa v[100:101], v101 src0_sel:WORD_1
	v_pk_fma_f32 v[64:65], v[176:177], s[16:17], v[64:65] op_sel_hi:[1,0,1]
	v_pk_fma_f32 v[178:179], v[26:27], v[180:181], v[178:179] op_sel_hi:[0,1,1]
	v_cvt_pk_f32_fp8_e32 v[180:181], v107
	v_cvt_pk_f32_fp8_sdwa v[106:107], v107 src0_sel:WORD_1
	v_pk_mul_f32 v[196:197], v[196:197], s[30:31] op_sel_hi:[1,0]
	v_pk_fma_f32 v[64:65], v[60:61], v[160:161], v[64:65] op_sel_hi:[0,1,1]
	v_cvt_pk_f32_fp8_e32 v[160:161], v182
	v_pk_fma_f32 v[222:223], v[2:3], v[232:233], v[222:223] op_sel_hi:[0,1,1]
	v_cvt_pk_f32_fp8_e32 v[232:233], v105
	v_cvt_pk_f32_fp8_sdwa v[104:105], v105 src0_sel:WORD_1
	v_pk_fma_f32 v[196:197], v[198:199], s[16:17], v[196:197] op_sel_hi:[1,0,1]
	v_cvt_pk_f32_fp8_e32 v[198:199], v184
	v_pk_fma_f32 v[218:219], v[4:5], v[218:219], v[222:223] op_sel_hi:[0,1,1]
	v_cvt_pk_f32_fp8_e32 v[222:223], v109
	v_pk_fma_f32 v[54:55], v[2:3], v[98:99], v[54:55] op_sel_hi:[0,1,1]
	v_cvt_pk_f32_fp8_e32 v[204:205], v186
	v_pk_fma_f32 v[54:55], v[4:5], v[100:101], v[54:55] op_sel_hi:[0,1,1]
	v_cvt_pk_f32_fp8_e32 v[212:213], v190
	v_pk_fma_f32 v[180:181], v[18:19], v[180:181], v[218:219] op_sel_hi:[0,1,1]
	v_pk_fma_f32 v[54:55], v[18:19], v[106:107], v[54:55] op_sel_hi:[0,1,1]
	v_cvt_pk_f32_fp8_e32 v[224:225], v192
	v_pk_fma_f32 v[180:181], v[20:21], v[232:233], v[180:181] op_sel_hi:[0,1,1]
	v_pk_fma_f32 v[54:55], v[20:21], v[104:105], v[54:55] op_sel_hi:[0,1,1]
	v_pk_fma_f32 v[104:105], v[2:3], v[160:161], v[188:189] op_sel_hi:[0,1,1]
	v_lshlrev_b32_e32 v174, 16, v175
	v_and_b32_e32 v175, 0xffff0000, v175
	v_pk_mul_f32 v[194:195], v[194:195], s[30:31] op_sel_hi:[1,0]
	v_pk_fma_f32 v[180:181], v[22:23], v[222:223], v[180:181] op_sel_hi:[0,1,1]
	v_cvt_pk_f32_fp8_e32 v[222:223], v152
	v_pk_fma_f32 v[104:105], v[4:5], v[198:199], v[104:105] op_sel_hi:[0,1,1]
	v_pk_fma_f32 v[174:175], v[174:175], s[16:17], v[194:195] op_sel_hi:[1,0,1]
	v_cvt_pk_f32_fp8_sdwa v[176:177], v182 src0_sel:WORD_1
	v_cvt_pk_f32_fp8_e32 v[98:99], v136
	v_pk_fma_f32 v[104:105], v[18:19], v[204:205], v[104:105] op_sel_hi:[0,1,1]
	v_pk_fma_f32 v[174:175], v[60:61], v[200:201], v[174:175] op_sel_hi:[0,1,1]
	v_cvt_pk_f32_fp8_sdwa v[200:201], v184 src0_sel:WORD_1
	v_cvt_pk_f32_fp8_e32 v[218:219], v117
	v_pk_fma_f32 v[104:105], v[20:21], v[212:213], v[104:105] op_sel_hi:[0,1,1]
	v_cvt_pk_f32_fp8_sdwa v[206:207], v186 src0_sel:WORD_1
	v_pk_fma_f32 v[104:105], v[22:23], v[224:225], v[104:105] op_sel_hi:[0,1,1]
	v_cvt_pk_f32_fp8_sdwa v[214:215], v190 src0_sel:WORD_1
	v_pk_fma_f32 v[104:105], v[24:25], v[222:223], v[104:105] op_sel_hi:[0,1,1]
	v_pk_fma_f32 v[6:7], v[2:3], v[8:9], v[6:7] op_sel_hi:[0,1,1]
	v_cvt_pk_f32_fp8_sdwa v[220:221], v192 src0_sel:WORD_1
	v_pk_fma_f32 v[98:99], v[26:27], v[98:99], v[104:105] op_sel_hi:[0,1,1]
	v_pk_fma_f32 v[104:105], v[2:3], v[176:177], v[174:175] op_sel_hi:[0,1,1]
	v_pk_fma_f32 v[6:7], v[4:5], v[12:13], v[6:7] op_sel_hi:[0,1,1]
	v_pk_fma_f32 v[180:181], v[24:25], v[218:219], v[180:181] op_sel_hi:[0,1,1]
	v_cvt_pk_f32_fp8_sdwa v[218:219], v152 src0_sel:WORD_1
	v_pk_fma_f32 v[104:105], v[4:5], v[200:201], v[104:105] op_sel_hi:[0,1,1]
	v_pk_fma_f32 v[6:7], v[18:19], v[114:115], v[6:7] op_sel_hi:[0,1,1]
	v_cvt_pk_f32_fp8_e32 v[194:195], v183
	v_cvt_pk_f32_fp8_sdwa v[100:101], v136 src0_sel:WORD_1
	v_pk_fma_f32 v[104:105], v[18:19], v[206:207], v[104:105] op_sel_hi:[0,1,1]
	v_pk_fma_f32 v[6:7], v[20:21], v[120:121], v[6:7] op_sel_hi:[0,1,1]
	v_pk_fma_f32 v[196:197], v[60:61], v[202:203], v[196:197] op_sel_hi:[0,1,1]
	v_cvt_pk_f32_fp8_e32 v[202:203], v185
	v_cvt_pk_f32_fp8_e32 v[232:233], v129
	v_pk_fma_f32 v[104:105], v[20:21], v[214:215], v[104:105] op_sel_hi:[0,1,1]
	v_pk_fma_f32 v[6:7], v[22:23], v[126:127], v[6:7] op_sel_hi:[0,1,1]
	v_cvt_pk_f32_fp8_e32 v[208:209], v187
	v_pk_fma_f32 v[104:105], v[22:23], v[220:221], v[104:105] op_sel_hi:[0,1,1]
	v_pk_fma_f32 v[6:7], v[24:25], v[134:135], v[6:7] op_sel_hi:[0,1,1]
	v_cvt_pk_f32_fp8_e32 v[216:217], v191
	v_pk_fma_f32 v[104:105], v[24:25], v[218:219], v[104:105] op_sel_hi:[0,1,1]
	v_pk_fma_f32 v[12:13], v[26:27], v[144:145], v[6:7] op_sel_hi:[0,1,1]
	v_pk_fma_f32 v[6:7], v[2:3], v[56:57], v[38:39] op_sel_hi:[0,1,1]
	v_cvt_pk_f32_fp8_e32 v[226:227], v193
	v_pk_fma_f32 v[100:101], v[26:27], v[100:101], v[104:105] op_sel_hi:[0,1,1]
	v_pk_fma_f32 v[104:105], v[2:3], v[194:195], v[196:197] op_sel_hi:[0,1,1]
	v_pk_fma_f32 v[6:7], v[4:5], v[70:71], v[6:7] op_sel_hi:[0,1,1]
	v_pk_fma_f32 v[180:181], v[26:27], v[232:233], v[180:181] op_sel_hi:[0,1,1]
	v_cvt_pk_f32_fp8_e32 v[232:233], v153
	v_pk_fma_f32 v[104:105], v[4:5], v[202:203], v[104:105] op_sel_hi:[0,1,1]
	v_pk_fma_f32 v[6:7], v[18:19], v[78:79], v[6:7] op_sel_hi:[0,1,1]
	v_cvt_pk_f32_fp8_sdwa v[182:183], v183 src0_sel:WORD_1
	v_cvt_pk_f32_fp8_e32 v[106:107], v137
	v_pk_fma_f32 v[104:105], v[18:19], v[208:209], v[104:105] op_sel_hi:[0,1,1]
	v_pk_fma_f32 v[6:7], v[20:21], v[84:85], v[6:7] op_sel_hi:[0,1,1]
	v_pk_fma_f32 v[104:105], v[20:21], v[216:217], v[104:105] op_sel_hi:[0,1,1]
	v_pk_fma_f32 v[6:7], v[22:23], v[88:89], v[6:7] op_sel_hi:[0,1,1]
	v_pk_fma_f32 v[104:105], v[22:23], v[226:227], v[104:105] op_sel_hi:[0,1,1]
	v_pk_fma_f32 v[6:7], v[24:25], v[92:93], v[6:7] op_sel_hi:[0,1,1]
	v_pk_fma_f32 v[104:105], v[24:25], v[232:233], v[104:105] op_sel_hi:[0,1,1]
	v_pk_fma_f32 v[38:39], v[26:27], v[94:95], v[6:7] op_sel_hi:[0,1,1]
	v_pk_fma_f32 v[104:105], v[26:27], v[106:107], v[104:105] op_sel_hi:[0,1,1]
	v_pk_fma_f32 v[64:65], v[2:3], v[182:183], v[64:65] op_sel_hi:[0,1,1]
	v_pk_fma_f32 v[102:103], v[2:3], v[138:139], v[102:103] op_sel_hi:[0,1,1]
	v_pk_fma_f32 v[106:107], v[2:3], v[122:123], v[110:111] op_sel_hi:[0,1,1]
	v_pk_fma_f32 v[30:31], v[2:3], v[112:113], v[30:31] op_sel_hi:[0,1,1]
	v_add_f32_e32 v3, 0, v38
	v_add_f32_e32 v3, v39, v3
	v_pk_fma_f32 v[6:7], v[2:3], v[44:45], v[36:37] op_sel_hi:[0,1,1]
	v_pk_fma_f32 v[6:7], v[4:5], v[52:53], v[6:7] op_sel_hi:[0,1,1]
	v_pk_fma_f32 v[6:7], v[18:19], v[66:67], v[6:7] op_sel_hi:[0,1,1]
	v_pk_fma_f32 v[6:7], v[20:21], v[76:77], v[6:7] op_sel_hi:[0,1,1]
	v_pk_fma_f32 v[6:7], v[22:23], v[82:83], v[6:7] op_sel_hi:[0,1,1]
	v_pk_fma_f32 v[6:7], v[24:25], v[86:87], v[6:7] op_sel_hi:[0,1,1]
	v_pk_fma_f32 v[36:37], v[26:27], v[90:91], v[6:7] op_sel_hi:[0,1,1]
	v_add_f32_e32 v3, v36, v3
	v_add_f32_e32 v3, v37, v3
	v_pk_fma_f32 v[6:7], v[2:3], v[32:33], v[16:17] op_sel_hi:[0,1,1]
	v_pk_fma_f32 v[6:7], v[4:5], v[40:41], v[6:7] op_sel_hi:[0,1,1]
	v_pk_fma_f32 v[6:7], v[18:19], v[48:49], v[6:7] op_sel_hi:[0,1,1]
	v_pk_fma_f32 v[6:7], v[20:21], v[58:59], v[6:7] op_sel_hi:[0,1,1]
	v_cvt_pk_f32_fp8_sdwa v[184:185], v185 src0_sel:WORD_1
	v_pk_fma_f32 v[6:7], v[22:23], v[68:69], v[6:7] op_sel_hi:[0,1,1]
	v_pk_fma_f32 v[6:7], v[24:25], v[74:75], v[6:7] op_sel_hi:[0,1,1]
	v_pk_fma_f32 v[16:17], v[26:27], v[80:81], v[6:7] op_sel_hi:[0,1,1]
	v_add_f32_e32 v3, v16, v3
	v_pk_fma_f32 v[64:65], v[4:5], v[184:185], v[64:65] op_sel_hi:[0,1,1]
	v_pk_fma_f32 v[102:103], v[4:5], v[146:147], v[102:103] op_sel_hi:[0,1,1]
	v_pk_fma_f32 v[106:107], v[4:5], v[130:131], v[106:107] op_sel_hi:[0,1,1]
	v_pk_fma_f32 v[30:31], v[4:5], v[118:119], v[30:31] op_sel_hi:[0,1,1]
	v_add_f32_e32 v5, v17, v3
	v_pk_fma_f32 v[2:3], v[2:3], v[28:29], v[14:15] op_sel_hi:[0,1,1]
	v_pk_fma_f32 v[2:3], v[4:5], v[34:35], v[2:3] op_sel_hi:[0,1,1]
	v_pk_fma_f32 v[2:3], v[18:19], v[42:43], v[2:3] op_sel_hi:[0,1,1]
	v_pk_fma_f32 v[2:3], v[20:21], v[46:47], v[2:3] op_sel_hi:[0,1,1]
	v_pk_fma_f32 v[102:103], v[18:19], v[154:155], v[102:103] op_sel_hi:[0,1,1]
	v_pk_fma_f32 v[2:3], v[22:23], v[50:51], v[2:3] op_sel_hi:[0,1,1]
	v_pk_fma_f32 v[102:103], v[20:21], v[162:163], v[102:103] op_sel_hi:[0,1,1]
	v_pk_fma_f32 v[2:3], v[24:25], v[62:63], v[2:3] op_sel_hi:[0,1,1]
	v_pk_fma_f32 v[102:103], v[22:23], v[166:167], v[102:103] op_sel_hi:[0,1,1]
	v_pk_fma_f32 v[106:107], v[18:19], v[140:141], v[106:107] op_sel_hi:[0,1,1]
	v_pk_fma_f32 v[14:15], v[26:27], v[72:73], v[2:3] op_sel_hi:[0,1,1]
	v_pk_fma_f32 v[102:103], v[24:25], v[170:171], v[102:103] op_sel_hi:[0,1,1]
	v_pk_fma_f32 v[106:107], v[20:21], v[148:149], v[106:107] op_sel_hi:[0,1,1]
	v_add_f32_e32 v2, v14, v5
	v_pk_fma_f32 v[102:103], v[26:27], v[172:173], v[102:103] op_sel_hi:[0,1,1]
	v_pk_fma_f32 v[106:107], v[22:23], v[156:157], v[106:107] op_sel_hi:[0,1,1]
	v_pk_fma_f32 v[30:31], v[18:19], v[124:125], v[30:31] op_sel_hi:[0,1,1]
	v_add_f32_e32 v2, v15, v2
	v_pk_fma_f32 v[106:107], v[24:25], v[164:165], v[106:107] op_sel_hi:[0,1,1]
	v_pk_fma_f32 v[30:31], v[20:21], v[132:133], v[30:31] op_sel_hi:[0,1,1]
	v_add_f32_e32 v2, v2, v102
	v_pk_fma_f32 v[106:107], v[26:27], v[168:169], v[106:107] op_sel_hi:[0,1,1]
	v_pk_fma_f32 v[30:31], v[22:23], v[142:143], v[30:31] op_sel_hi:[0,1,1]
	v_add_f32_e32 v2, v103, v2
	v_pk_fma_f32 v[30:31], v[24:25], v[150:151], v[30:31] op_sel_hi:[0,1,1]
	v_add_f32_e32 v2, v106, v2
	v_pk_fma_f32 v[30:31], v[26:27], v[158:159], v[30:31] op_sel_hi:[0,1,1]
	v_add_f32_e32 v2, v107, v2
	v_add_f32_e32 v2, v30, v2
	v_cvt_pk_f32_fp8_sdwa v[186:187], v187 src0_sel:WORD_1
	v_add_f32_e32 v2, v31, v2
	v_cvt_pk_f32_fp8_sdwa v[190:191], v191 src0_sel:WORD_1
	v_add_f32_e32 v2, v12, v2
	v_cvt_pk_f32_fp8_sdwa v[192:193], v193 src0_sel:WORD_1
	v_add_f32_e32 v2, v13, v2
	v_cvt_pk_f32_fp8_sdwa v[152:153], v153 src0_sel:WORD_1
	v_add_f32_e32 v2, v2, v98
	v_cvt_pk_f32_fp8_sdwa v[136:137], v137 src0_sel:WORD_1
	v_pk_fma_f32 v[64:65], v[18:19], v[186:187], v[64:65] op_sel_hi:[0,1,1]
	v_add_f32_e32 v2, v99, v2
	v_pk_fma_f32 v[64:65], v[20:21], v[190:191], v[64:65] op_sel_hi:[0,1,1]
	v_add_f32_e32 v2, v100, v2
	v_pk_fma_f32 v[64:65], v[22:23], v[192:193], v[64:65] op_sel_hi:[0,1,1]
	v_add_f32_e32 v2, v101, v2
	v_pk_fma_f32 v[64:65], v[24:25], v[152:153], v[64:65] op_sel_hi:[0,1,1]
	v_add_f32_e32 v2, v104, v2
	v_pk_fma_f32 v[64:65], v[26:27], v[136:137], v[64:65] op_sel_hi:[0,1,1]
	v_add_f32_e32 v2, v105, v2
	v_add_f32_e32 v2, v64, v2
	v_cvt_pk_f32_fp8_sdwa v[108:109], v109 src0_sel:WORD_1
	v_add_f32_e32 v2, v65, v2
	v_cvt_pk_f32_fp8_sdwa v[116:117], v117 src0_sel:WORD_1
	v_add_f32_e32 v2, v2, v96
	v_cvt_pk_f32_fp8_sdwa v[128:129], v129 src0_sel:WORD_1
	v_add_f32_e32 v2, v97, v2
	v_add_f32_e32 v2, v178, v2
	v_pk_fma_f32 v[54:55], v[22:23], v[108:109], v[54:55] op_sel_hi:[0,1,1]
	v_add_f32_e32 v2, v179, v2
	v_pk_fma_f32 v[54:55], v[24:25], v[116:117], v[54:55] op_sel_hi:[0,1,1]
	v_add_f32_e32 v2, v180, v2
	v_pk_fma_f32 v[54:55], v[26:27], v[128:129], v[54:55] op_sel_hi:[0,1,1]
	v_add_f32_e32 v2, v181, v2
	v_add_f32_e32 v2, v54, v2
	v_add_f32_e32 v2, v55, v2
	v_lshlrev_b32_e32 v34, 5, v23
	v_readlane_b32 s100, v254, 23
	s_add_i32 s100, s100, s50
	s_add_i32 s100, s100, -7
	s_lshl_b32 s100, s100, 2
	v_mov_b32_e32 v60, s100
	v_add_u32_e32 v94, 0x100000, v60
	v_add_u32_e32 v95, 0x1000, v34
	global_load_dwordx4 v[194:197], v94, s[20:21]
	global_load_dwordx4 v[198:201], v94, s[20:21] offset:16
	global_load_dwordx4 v[202:205], v60, s[20:21]
	global_load_dwordx4 v[206:209], v60, s[20:21] offset:16
	global_load_dwordx4 v[90:93], v34, s[4:5]
	global_load_dwordx4 v[108:111], v34, s[4:5] offset:16
	global_load_dwordx4 v[112:115], v34, s[6:7]
	global_load_dwordx4 v[116:119], v34, s[6:7] offset:16
	global_load_dwordx4 v[120:123], v34, s[4:5] offset:2048
	global_load_dwordx4 v[124:127], v34, s[4:5] offset:2064
	global_load_dwordx4 v[128:131], v34, s[6:7] offset:2048
	global_load_dwordx4 v[132:135], v34, s[6:7] offset:2064
	global_load_dwordx4 v[136:139], v95, s[4:5]
	global_load_dwordx4 v[140:143], v95, s[4:5] offset:16
	global_load_dwordx4 v[144:147], v95, s[6:7]
	global_load_dwordx4 v[148:151], v95, s[6:7] offset:16
	global_load_dwordx4 v[152:155], v95, s[4:5] offset:2048
	global_load_dwordx4 v[156:159], v95, s[4:5] offset:2064
	global_load_dwordx4 v[160:163], v95, s[6:7] offset:2048
	global_load_dwordx4 v[164:167], v95, s[6:7] offset:2064
	ds_swizzle_b32 v3, v2 offset:swizzle(SWAP,1)
	s_add_u32 s56, s8, s54
	v_mov_b32_e32 v35, v1
	s_addc_u32 s57, s9, s55
	s_waitcnt lgkmcnt(0)
	v_add_f32_e32 v2, v2, v3
	ds_swizzle_b32 v3, v2 offset:swizzle(SWAP,2)
	s_waitcnt lgkmcnt(0)
	v_add_f32_e32 v2, v2, v3
	ds_swizzle_b32 v3, v2 offset:swizzle(SWAP,4)
	s_waitcnt lgkmcnt(0)
	v_add_f32_e32 v2, v2, v3
	ds_swizzle_b32 v3, v2 offset:swizzle(SWAP,8)
	s_waitcnt lgkmcnt(0)
	v_add_f32_e32 v18, v2, v3
	ds_swizzle_b32 v19, v18 offset:swizzle(SWAP,16)
	s_waitcnt lgkmcnt(0)
	v_add_f32_e32 v18, v18, v19
	v_mov_b32_e32 v19, v18
	s_nop 1
	v_permlane32_swap_b32_e32 v18, v19
	v_add_f32_e32 v18, v18, v19
	v_mul_f32_e32 v20, 0x3a000000, v18
	v_pk_add_f32 v[22:23], v[38:39], v[20:21] op_sel_hi:[1,0] neg_lo:[0,1] neg_hi:[0,1]
	v_pk_add_f32 v[36:37], v[36:37], v[20:21] op_sel_hi:[1,0] neg_lo:[0,1] neg_hi:[0,1]
	v_pk_mul_f32 v[24:25], v[22:23], v[22:23]
	v_pk_mul_f32 v[56:57], v[36:37], v[36:37]
	v_add_f32_e32 v24, v24, v25
	v_pk_add_f32 v[58:59], v[16:17], v[20:21] op_sel_hi:[1,0] neg_lo:[0,1] neg_hi:[0,1]
	v_add_f32_e32 v24, v56, v24
	v_pk_mul_f32 v[62:63], v[58:59], v[58:59]
	v_add_f32_e32 v24, v57, v24
	v_pk_add_f32 v[66:67], v[14:15], v[20:21] op_sel_hi:[1,0] neg_lo:[0,1] neg_hi:[0,1]
	v_add_f32_e32 v24, v62, v24
	v_pk_mul_f32 v[68:69], v[66:67], v[66:67]
	v_add_f32_e32 v24, v63, v24
	v_pk_add_f32 v[38:39], v[102:103], v[20:21] op_sel_hi:[1,0] neg_lo:[0,1] neg_hi:[0,1]
	v_add_f32_e32 v24, v68, v24
	v_pk_mul_f32 v[70:71], v[38:39], v[38:39]
	v_add_f32_e32 v24, v69, v24
	v_pk_add_f32 v[40:41], v[106:107], v[20:21] op_sel_hi:[1,0] neg_lo:[0,1] neg_hi:[0,1]
	v_add_f32_e32 v24, v70, v24
	v_pk_mul_f32 v[72:73], v[40:41], v[40:41]
	v_add_f32_e32 v24, v71, v24
	v_pk_add_f32 v[42:43], v[30:31], v[20:21] op_sel_hi:[1,0] neg_lo:[0,1] neg_hi:[0,1]
	v_add_f32_e32 v24, v72, v24
	v_pk_mul_f32 v[74:75], v[42:43], v[42:43]
	v_add_f32_e32 v24, v73, v24
	v_pk_add_f32 v[44:45], v[12:13], v[20:21] op_sel_hi:[1,0] neg_lo:[0,1] neg_hi:[0,1]
	v_add_f32_e32 v24, v74, v24
	v_pk_mul_f32 v[76:77], v[44:45], v[44:45]
	v_add_f32_e32 v24, v75, v24
	v_pk_add_f32 v[30:31], v[98:99], v[20:21] op_sel_hi:[1,0] neg_lo:[0,1] neg_hi:[0,1]
	v_add_f32_e32 v24, v76, v24
	v_pk_mul_f32 v[78:79], v[30:31], v[30:31]
	v_add_f32_e32 v24, v77, v24
	v_pk_add_f32 v[32:33], v[100:101], v[20:21] op_sel_hi:[1,0] neg_lo:[0,1] neg_hi:[0,1]
	v_add_f32_e32 v24, v78, v24
	v_pk_mul_f32 v[80:81], v[32:33], v[32:33]
	v_add_f32_e32 v24, v79, v24
	v_pk_add_f32 v[26:27], v[104:105], v[20:21] op_sel_hi:[1,0] neg_lo:[0,1] neg_hi:[0,1]
	v_add_f32_e32 v24, v80, v24
	v_pk_mul_f32 v[82:83], v[26:27], v[26:27]
	v_add_f32_e32 v24, v81, v24
	v_pk_add_f32 v[28:29], v[64:65], v[20:21] op_sel_hi:[1,0] neg_lo:[0,1] neg_hi:[0,1]
	v_add_f32_e32 v24, v82, v24
	v_pk_mul_f32 v[64:65], v[28:29], v[28:29]
	v_add_f32_e32 v24, v83, v24
	v_pk_add_f32 v[16:17], v[96:97], v[20:21] op_sel_hi:[1,0] neg_lo:[0,1] neg_hi:[0,1]
	v_add_f32_e32 v24, v64, v24
	v_pk_mul_f32 v[84:85], v[16:17], v[16:17]
	v_add_f32_e32 v24, v65, v24
	v_pk_add_f32 v[18:19], v[178:179], v[20:21] op_sel_hi:[1,0] neg_lo:[0,1] neg_hi:[0,1]
	v_add_f32_e32 v24, v84, v24
	v_pk_mul_f32 v[86:87], v[18:19], v[18:19]
	v_add_f32_e32 v24, v85, v24
	v_pk_add_f32 v[12:13], v[180:181], v[20:21] op_sel_hi:[1,0] neg_lo:[0,1] neg_hi:[0,1]
	v_add_f32_e32 v24, v86, v24
	v_pk_mul_f32 v[88:89], v[12:13], v[12:13]
	v_add_f32_e32 v24, v87, v24
	v_pk_add_f32 v[14:15], v[54:55], v[20:21] op_sel_hi:[1,0] neg_lo:[0,1] neg_hi:[0,1]
	v_add_f32_e32 v24, v88, v24
	v_pk_mul_f32 v[20:21], v[14:15], v[14:15]
	v_add_f32_e32 v24, v89, v24
	v_add_f32_e32 v20, v20, v24
	v_add_f32_e32 v20, v21, v20
	s_nop 1
	s_waitcnt lgkmcnt(0)
	v_add_f32_dpp v20, v20, v20 quad_perm:[1,0,3,2] row_mask:0xf bank_mask:0xf
	s_nop 1
	s_waitcnt lgkmcnt(0)
	v_add_f32_dpp v20, v20, v20 quad_perm:[2,3,0,1] row_mask:0xf bank_mask:0xf
	s_nop 1
	s_waitcnt lgkmcnt(0)
	v_add_f32_dpp v20, v20, v20 row_half_mirror row_mask:0xf bank_mask:0xf
	s_nop 1
	s_waitcnt lgkmcnt(0)
	v_add_f32_dpp v20, v20, v20 row_mirror row_mask:0xf bank_mask:0xf
	ds_swizzle_b32 v21, v20 offset:swizzle(SWAP,16)
	s_waitcnt lgkmcnt(0)
	v_add_f32_e32 v20, v20, v21
	v_mov_b32_e32 v21, v20
	s_nop 1
	v_permlane32_swap_b32_e32 v20, v21
	v_add_f32_e32 v20, v20, v21
	v_fmamk_f32 v20, v20, 0x3a000000, v210
	v_mul_f32_e32 v21, 0x4f800000, v20
	v_cmp_gt_f32_e32 vcc, s25, v20
	s_nop 1
	v_cndmask_b32_e32 v20, v20, v21, vcc
	v_sqrt_f32_e32 v21, v20
	s_nop 0
	v_add_u32_e32 v24, -1, v21
	v_fma_f32 v25, -v24, v21, v20
	v_cmp_ge_f32_e64 s[38:39], 0, v25
	v_add_u32_e32 v25, 1, v21
	s_nop 0
	v_cndmask_b32_e64 v24, v21, v24, s[38:39]
	v_fma_f32 v21, -v25, v21, v20
	v_cmp_lt_f32_e64 s[38:39], 0, v21
	s_nop 1
	v_cndmask_b32_e64 v21, v24, v25, s[38:39]
	v_mul_f32_e32 v24, 0x37800000, v21
	v_cndmask_b32_e32 v21, v21, v24, vcc
	v_cmp_class_f32_e32 vcc, v20, v211
	s_nop 1
	v_cndmask_b32_e32 v24, v21, v20, vcc
	v_div_scale_f32 v25, s[38:39], v24, v24, 1.0
	v_rcp_f32_e32 v54, v25
	v_lshl_add_u64 v[20:21], s[56:57], 0, v[34:35]
	s_add_u32 s56, s10, s48
	s_addc_u32 s57, s11, s49
	v_fma_f32 v55, -v25, v54, 1.0
	v_fmac_f32_e32 v54, v55, v54
	v_div_scale_f32 v55, vcc, 1.0, v24, 1.0
	v_mul_f32_e32 v56, v55, v54
	v_fma_f32 v57, -v25, v56, v55
	v_fmac_f32_e32 v56, v57, v54
	v_fma_f32 v25, -v25, v56, v55
	v_div_fmas_f32 v25, v25, v54, v56
	v_div_fixup_f32 v24, v25, v24, 1.0
	v_pk_mul_f32 v[22:23], v[22:23], v[24:25] op_sel_hi:[1,0]
	s_andn2_b64 vcc, exec, s[40:41]
	s_waitcnt vmcnt(12)
	v_pk_fma_f32 v[6:7], v[90:91], v[22:23], v[112:113]
	v_pk_mul_f32 v[22:23], v[36:37], v[24:25] op_sel_hi:[1,0]
	s_nop 0
	v_pk_fma_f32 v[8:9], v[92:93], v[22:23], v[114:115]
	v_pk_mul_f32 v[22:23], v[58:59], v[24:25] op_sel_hi:[1,0]
	s_nop 0
	v_pk_fma_f32 v[2:3], v[108:109], v[22:23], v[116:117]
	v_pk_mul_f32 v[22:23], v[66:67], v[24:25] op_sel_hi:[1,0]
	s_nop 0
	v_pk_fma_f32 v[4:5], v[110:111], v[22:23], v[118:119]
	v_cndmask_b32_e64 v22, 0, 1, s[40:41]
	v_cmp_ne_u32_e64 s[38:39], 1, v22
	s_cbranch_vccnz .LBB0_1357
	s_mov_b64 s[58:59], 0
	global_store_dwordx4 v[20:21], v[6:9], off
	global_store_dwordx4 v[20:21], v[2:5], off offset:16
